# speedup vs baseline: 1.0023x; 1.0023x over previous
_Z11pwconv_mfmaPKfPK15HIP_vector_typeIjLj4EES0_Pf:
	s_memrealtime s[52:53]
	s_load_dwordx4 s[12:15], s[0:1], 0x0
	s_load_dwordx4 s[16:19], s[0:1], 0x10
	s_and_b32 s20, s2, 7
	s_lshr_b32 s21, s2, 3
	v_lshrrev_b32_e32 v1, 6, v0
	v_and_b32_e32 v2, 63, v0
	s_nop 0
	v_readfirstlane_b32 s22, v1
	s_nop 3
	s_lshl_b32 s23, s20, 3
	s_add_i32 s23, s23, s22
	s_mul_i32 s24, s23, 0x439200
	s_mul_i32 s25, s21, 0x1f0
	s_add_u32 s24, s24, s25
	s_lshl_b32 s25, s21, 17
	s_lshl_b32 s26, s22, 13
	s_add_u32 s25, s25, s26
	s_mul_i32 s27, s20, 0x1e080
	s_mul_i32 s36, s21, 0x1f0
	s_add_u32 s27, s27, s36
	v_min_u32_e32 v10, 61, v2
	v_lshlrev_b32_e32 v3, 3, v10
	v_lshlrev_b32_e32 v4, 4, v2
	v_cmp_lt_u32_e32 vcc, 30, v10
	s_nop 1
	v_cndmask_b32_e64 v5, 0, 1, vcc
	v_mul_u32_u24_e32 v6, 31, v5
	v_sub_u32_e32 v6, v10, v6
	v_lshl_add_u32 v7, v1, 1, v5
	v_and_b32_e32 v8, 7, v6
	v_xor_b32_e32 v7, v7, v8
	v_lshlrev_b32_e32 v7, 4, v7
	v_lshl_add_u32 v5, v6, 12, v7
	s_lshl_b32 s36, s22, 2
	s_add_i32 s36, s36, 0
	s_and_b32 s36, s36, 7
	s_lshl_b32 s37, s22, 14
	s_add_i32 s37, s37, 0x0
	v_xor_b32_e32 v6, s36, v2
	v_lshlrev_b32_e32 v6, 4, v6
	v_add_u32_e32 v6, s37, v6
	s_lshl_b32 s36, s22, 2
	s_add_i32 s36, s36, 1
	s_and_b32 s36, s36, 7
	s_lshl_b32 s37, s22, 14
	s_add_i32 s37, s37, 0x1000
	v_xor_b32_e32 v7, s36, v2
	v_lshlrev_b32_e32 v7, 4, v7
	v_add_u32_e32 v7, s37, v7
	s_lshl_b32 s36, s22, 2
	s_add_i32 s36, s36, 2
	s_and_b32 s36, s36, 7
	s_lshl_b32 s37, s22, 14
	s_add_i32 s37, s37, 0x2000
	v_xor_b32_e32 v8, s36, v2
	v_lshlrev_b32_e32 v8, 4, v8
	v_add_u32_e32 v8, s37, v8
	s_lshl_b32 s36, s22, 2
	s_add_i32 s36, s36, 3
	s_and_b32 s36, s36, 7
	s_lshl_b32 s37, s22, 14
	s_add_i32 s37, s37, 0x3000
	v_xor_b32_e32 v9, s36, v2
	v_lshlrev_b32_e32 v9, 4, v9
	v_add_u32_e32 v9, s37, v9
	v_lshrrev_b32_e32 v10, 5, v0
	v_lshrrev_b32_e32 v11, 1, v10
	v_mul_u32_u24_e32 v11, 0x3c10, v11
	v_and_b32_e32 v10, 1, v10
	v_mul_u32_u24_e32 v10, 0xf8, v10
	v_add_u32_e32 v11, v11, v10
	v_and_b32_e32 v10, 31, v0
	v_lshl_add_u32 v11, v10, 3, v11
	v_add_u32_e32 v11, s27, v11
	v_cmp_eq_u32_e32 vcc, 31, v10
	v_mov_b32_e32 v10, 0x7f000000
	s_nop 1
	v_cndmask_b32_e32 v11, v11, v10, vcc
	s_waitcnt lgkmcnt(0)
	s_add_u32 s4, s12, s24
	s_addc_u32 s5, s13, 0
	s_and_b32 s5, s5, 0xffff
	s_sub_u32 s6, 0x10e48000, s24
	s_mov_b32 s7, 0x20000
	s_add_u32 s8, s14, s25
	s_addc_u32 s9, s15, 0
	s_and_b32 s9, s9, 0xffff
	s_sub_u32 s10, 0x400000, s25
	s_mov_b32 s11, 0x20000
	s_mov_b32 s28, s16
	s_and_b32 s29, s17, 0xffff
	s_mov_b32 s30, 0xf0400
	s_mov_b32 s31, 0x20000
	s_mov_b32 s32, s18
	s_and_b32 s33, s19, 0xffff
	s_mov_b32 s34, 0xf04000
	s_mov_b32 s35, 0x20000
	s_mov_b32 s40, 0x0
	s_mov_b32 s41, 0x21c90
	s_mov_b32 s42, 0x43920
	s_mov_b32 s43, 0x655b0
	s_mov_b32 s44, 0x87240
	s_mov_b32 s45, 0xa8ed0
	s_mov_b32 s46, 0xcab60
	s_mov_b32 s47, 0xec7f0
	buffer_load_dwordx2 v[44:45], v3, s[4:7], s40 offen nt
	buffer_load_dwordx2 v[46:47], v3, s[4:7], s41 offen nt
	buffer_load_dwordx2 v[48:49], v3, s[4:7], s42 offen nt
	buffer_load_dwordx2 v[50:51], v3, s[4:7], s43 offen nt
	buffer_load_dwordx2 v[52:53], v3, s[4:7], s44 offen nt
	buffer_load_dwordx2 v[54:55], v3, s[4:7], s45 offen nt
	buffer_load_dwordx2 v[56:57], v3, s[4:7], s46 offen nt
	buffer_load_dwordx2 v[58:59], v3, s[4:7], s47 offen nt
	s_mov_b32 s40, 0x10e480
	s_mov_b32 s41, 0x130110
	s_mov_b32 s42, 0x151da0
	s_mov_b32 s43, 0x173a30
	s_mov_b32 s44, 0x1956c0
	s_mov_b32 s45, 0x1b7350
	s_mov_b32 s46, 0x1d8fe0
	s_mov_b32 s47, 0x1fac70
	buffer_load_dwordx2 v[60:61], v3, s[4:7], s40 offen nt
	buffer_load_dwordx2 v[62:63], v3, s[4:7], s41 offen nt
	buffer_load_dwordx2 v[64:65], v3, s[4:7], s42 offen nt
	buffer_load_dwordx2 v[66:67], v3, s[4:7], s43 offen nt
	buffer_load_dwordx2 v[68:69], v3, s[4:7], s44 offen nt
	buffer_load_dwordx2 v[70:71], v3, s[4:7], s45 offen nt
	buffer_load_dwordx2 v[72:73], v3, s[4:7], s46 offen nt
	buffer_load_dwordx2 v[74:75], v3, s[4:7], s47 offen nt
	s_mov_b32 s40, 0x21c900
	s_mov_b32 s41, 0x23e590
	s_mov_b32 s42, 0x260220
	s_mov_b32 s43, 0x281eb0
	s_mov_b32 s44, 0x2a3b40
	s_mov_b32 s45, 0x2c57d0
	s_mov_b32 s46, 0x2e7460
	s_mov_b32 s47, 0x3090f0
	buffer_load_dwordx2 v[76:77], v3, s[4:7], s40 offen nt
	buffer_load_dwordx2 v[78:79], v3, s[4:7], s41 offen nt
	buffer_load_dwordx2 v[80:81], v3, s[4:7], s42 offen nt
	buffer_load_dwordx2 v[82:83], v3, s[4:7], s43 offen nt
	buffer_load_dwordx2 v[84:85], v3, s[4:7], s44 offen nt
	buffer_load_dwordx2 v[86:87], v3, s[4:7], s45 offen nt
	buffer_load_dwordx2 v[88:89], v3, s[4:7], s46 offen nt
	buffer_load_dwordx2 v[90:91], v3, s[4:7], s47 offen nt
	s_mov_b32 s40, 0x32ad80
	s_mov_b32 s41, 0x34ca10
	s_mov_b32 s42, 0x36e6a0
	s_mov_b32 s43, 0x390330
	s_mov_b32 s44, 0x3b1fc0
	s_mov_b32 s45, 0x3d3c50
	s_mov_b32 s46, 0x3f58e0
	s_mov_b32 s47, 0x417570
	buffer_load_dwordx2 v[92:93], v3, s[4:7], s40 offen nt
	buffer_load_dwordx2 v[94:95], v3, s[4:7], s41 offen nt
	buffer_load_dwordx2 v[96:97], v3, s[4:7], s42 offen nt
	buffer_load_dwordx2 v[98:99], v3, s[4:7], s43 offen nt
	buffer_load_dwordx2 v[100:101], v3, s[4:7], s44 offen nt
	buffer_load_dwordx2 v[102:103], v3, s[4:7], s45 offen nt
	buffer_load_dwordx2 v[104:105], v3, s[4:7], s46 offen nt
	buffer_load_dwordx2 v[106:107], v3, s[4:7], s47 offen nt
	buffer_load_dwordx2 v[252:253], v11, s[28:31], 0 offen
	s_mov_b32 s40, 0x0
	s_mov_b32 s41, 0x400
	s_mov_b32 s42, 0x800
	s_mov_b32 s43, 0xc00
	s_mov_b32 s44, 0x1000
	buffer_load_dwordx4 v[108:111], v4, s[8:11], s40 offen
	buffer_load_dwordx4 v[112:115], v4, s[8:11], s41 offen
	buffer_load_dwordx4 v[116:119], v4, s[8:11], s42 offen
	buffer_load_dwordx4 v[120:123], v4, s[8:11], s43 offen
	buffer_load_dwordx4 v[124:127], v4, s[8:11], s44 offen
	s_mov_b32 s40, 0x1400
	s_mov_b32 s41, 0x1800
	s_mov_b32 s42, 0x1c00
	s_mov_b32 s43, 0x2000
	s_mov_b32 s44, 0x2400
	buffer_load_dwordx4 v[128:131], v4, s[8:11], s40 offen
	buffer_load_dwordx4 v[132:135], v4, s[8:11], s41 offen
	buffer_load_dwordx4 v[136:139], v4, s[8:11], s42 offen
	buffer_load_dwordx4 v[140:143], v4, s[8:11], s43 offen
	buffer_load_dwordx4 v[144:147], v4, s[8:11], s44 offen
	s_mov_b32 s40, 0x10000
	s_mov_b32 s41, 0x10400
	s_mov_b32 s42, 0x10800
	s_mov_b32 s43, 0x10c00
	s_mov_b32 s44, 0x11000
	buffer_load_dwordx4 v[148:151], v4, s[8:11], s40 offen
	buffer_load_dwordx4 v[152:155], v4, s[8:11], s41 offen
	buffer_load_dwordx4 v[156:159], v4, s[8:11], s42 offen
	buffer_load_dwordx4 v[160:163], v4, s[8:11], s43 offen
	buffer_load_dwordx4 v[164:167], v4, s[8:11], s44 offen
	s_mov_b32 s40, 0x11400
	s_mov_b32 s41, 0x11800
	s_mov_b32 s42, 0x11c00
	s_mov_b32 s43, 0x12000
	s_mov_b32 s44, 0x12400
	buffer_load_dwordx4 v[168:171], v4, s[8:11], s40 offen
	buffer_load_dwordx4 v[172:175], v4, s[8:11], s41 offen
	buffer_load_dwordx4 v[176:179], v4, s[8:11], s42 offen
	buffer_load_dwordx4 v[180:183], v4, s[8:11], s43 offen
	buffer_load_dwordx4 v[184:187], v4, s[8:11], s44 offen
	s_waitcnt vmcnt(45)
	v_cvt_pkrtz_f16_f32 v12, v44, v46
	v_cvt_pkrtz_f16_f32 v13, v48, v50
	v_cvt_pkrtz_f16_f32 v14, v52, v54
	v_cvt_pkrtz_f16_f32 v15, v56, v58
	v_cvt_pkrtz_f16_f32 v16, v45, v47
	v_cvt_pkrtz_f16_f32 v17, v49, v51
	v_cvt_pkrtz_f16_f32 v18, v53, v55
	v_cvt_pkrtz_f16_f32 v19, v57, v59
.Lpace_0:
	s_memrealtime s[54:55]
	s_waitcnt lgkmcnt(0)
	s_sub_u32 s54, s54, s52
	s_cmp_ge_u32 s54, 280
	s_cbranch_scc1 .Lgo_0
	s_sleep 2
	s_branch .Lpace_0
.Lgo_0:
	s_mov_b32 s40, 0x3c10
	s_mov_b32 s41, 0x258a0
	s_mov_b32 s42, 0x47530
	s_mov_b32 s43, 0x691c0
	s_mov_b32 s44, 0x8ae50
	s_mov_b32 s45, 0xacae0
	s_mov_b32 s46, 0xce770
	s_mov_b32 s47, 0xf0400
	buffer_load_dwordx2 v[44:45], v3, s[4:7], s40 offen nt
	buffer_load_dwordx2 v[46:47], v3, s[4:7], s41 offen nt
	buffer_load_dwordx2 v[48:49], v3, s[4:7], s42 offen nt
	buffer_load_dwordx2 v[50:51], v3, s[4:7], s43 offen nt
	buffer_load_dwordx2 v[52:53], v3, s[4:7], s44 offen nt
	buffer_load_dwordx2 v[54:55], v3, s[4:7], s45 offen nt
	buffer_load_dwordx2 v[56:57], v3, s[4:7], s46 offen nt
	buffer_load_dwordx2 v[58:59], v3, s[4:7], s47 offen nt
	ds_write_b128 v5, v[12:15] offset:0
	ds_write_b128 v5, v[16:19] offset:2048
	s_waitcnt vmcnt(45)
	v_cvt_pkrtz_f16_f32 v12, v60, v62
	v_cvt_pkrtz_f16_f32 v13, v64, v66
	v_cvt_pkrtz_f16_f32 v14, v68, v70
	v_cvt_pkrtz_f16_f32 v15, v72, v74
	v_cvt_pkrtz_f16_f32 v16, v61, v63
	v_cvt_pkrtz_f16_f32 v17, v65, v67
	v_cvt_pkrtz_f16_f32 v18, v69, v71
	v_cvt_pkrtz_f16_f32 v19, v73, v75
.Lpace_1:
	s_memrealtime s[54:55]
	s_waitcnt lgkmcnt(0)
	s_sub_u32 s54, s54, s52
	s_cmp_ge_u32 s54, 415
	s_cbranch_scc1 .Lgo_1
	s_sleep 2
	s_branch .Lpace_1
.Lgo_1:
	s_mov_b32 s40, 0x112090
	s_mov_b32 s41, 0x133d20
	s_mov_b32 s42, 0x1559b0
	s_mov_b32 s43, 0x177640
	s_mov_b32 s44, 0x1992d0
	s_mov_b32 s45, 0x1baf60
	s_mov_b32 s46, 0x1dcbf0
	s_mov_b32 s47, 0x1fe880
	buffer_load_dwordx2 v[60:61], v3, s[4:7], s40 offen nt
	buffer_load_dwordx2 v[62:63], v3, s[4:7], s41 offen nt
	buffer_load_dwordx2 v[64:65], v3, s[4:7], s42 offen nt
	buffer_load_dwordx2 v[66:67], v3, s[4:7], s43 offen nt
	buffer_load_dwordx2 v[68:69], v3, s[4:7], s44 offen nt
	buffer_load_dwordx2 v[70:71], v3, s[4:7], s45 offen nt
	buffer_load_dwordx2 v[72:73], v3, s[4:7], s46 offen nt
	buffer_load_dwordx2 v[74:75], v3, s[4:7], s47 offen nt
	ds_write_b128 v5, v[12:15] offset:256
	ds_write_b128 v5, v[16:19] offset:2304
	s_waitcnt vmcnt(45)
	v_cvt_pkrtz_f16_f32 v12, v76, v78
	v_cvt_pkrtz_f16_f32 v13, v80, v82
	v_cvt_pkrtz_f16_f32 v14, v84, v86
	v_cvt_pkrtz_f16_f32 v15, v88, v90
	v_cvt_pkrtz_f16_f32 v16, v77, v79
	v_cvt_pkrtz_f16_f32 v17, v81, v83
	v_cvt_pkrtz_f16_f32 v18, v85, v87
	v_cvt_pkrtz_f16_f32 v19, v89, v91
.Lpace_2:
	s_memrealtime s[54:55]
	s_waitcnt lgkmcnt(0)
	s_sub_u32 s54, s54, s52
	s_cmp_ge_u32 s54, 550
	s_cbranch_scc1 .Lgo_2
	s_sleep 2
	s_branch .Lpace_2
.Lgo_2:
	s_mov_b32 s40, 0x220510
	s_mov_b32 s41, 0x2421a0
	s_mov_b32 s42, 0x263e30
	s_mov_b32 s43, 0x285ac0
	s_mov_b32 s44, 0x2a7750
	s_mov_b32 s45, 0x2c93e0
	s_mov_b32 s46, 0x2eb070
	s_mov_b32 s47, 0x30cd00
	buffer_load_dwordx2 v[76:77], v3, s[4:7], s40 offen nt
	buffer_load_dwordx2 v[78:79], v3, s[4:7], s41 offen nt
	buffer_load_dwordx2 v[80:81], v3, s[4:7], s42 offen nt
	buffer_load_dwordx2 v[82:83], v3, s[4:7], s43 offen nt
	buffer_load_dwordx2 v[84:85], v3, s[4:7], s44 offen nt
	buffer_load_dwordx2 v[86:87], v3, s[4:7], s45 offen nt
	buffer_load_dwordx2 v[88:89], v3, s[4:7], s46 offen nt
	buffer_load_dwordx2 v[90:91], v3, s[4:7], s47 offen nt
	ds_write_b128 v5, v[12:15] offset:512
	ds_write_b128 v5, v[16:19] offset:2560
	s_waitcnt vmcnt(45)
	v_cvt_pkrtz_f16_f32 v12, v92, v94
	v_cvt_pkrtz_f16_f32 v13, v96, v98
	v_cvt_pkrtz_f16_f32 v14, v100, v102
	v_cvt_pkrtz_f16_f32 v15, v104, v106
	v_cvt_pkrtz_f16_f32 v16, v93, v95
	v_cvt_pkrtz_f16_f32 v17, v97, v99
	v_cvt_pkrtz_f16_f32 v18, v101, v103
	v_cvt_pkrtz_f16_f32 v19, v105, v107
.Lpace_3:
	s_memrealtime s[54:55]
	s_waitcnt lgkmcnt(0)
	s_sub_u32 s54, s54, s52
	s_cmp_ge_u32 s54, 685
	s_cbranch_scc1 .Lgo_3
	s_sleep 2
	s_branch .Lpace_3
.Lgo_3:
	s_mov_b32 s40, 0x32e990
	s_mov_b32 s41, 0x350620
	s_mov_b32 s42, 0x3722b0
	s_mov_b32 s43, 0x393f40
	s_mov_b32 s44, 0x3b5bd0
	s_mov_b32 s45, 0x3d7860
	s_mov_b32 s46, 0x3f94f0
	s_mov_b32 s47, 0x41b180
	buffer_load_dwordx2 v[92:93], v3, s[4:7], s40 offen nt
	buffer_load_dwordx2 v[94:95], v3, s[4:7], s41 offen nt
	buffer_load_dwordx2 v[96:97], v3, s[4:7], s42 offen nt
	buffer_load_dwordx2 v[98:99], v3, s[4:7], s43 offen nt
	buffer_load_dwordx2 v[100:101], v3, s[4:7], s44 offen nt
	buffer_load_dwordx2 v[102:103], v3, s[4:7], s45 offen nt
	buffer_load_dwordx2 v[104:105], v3, s[4:7], s46 offen nt
	buffer_load_dwordx2 v[106:107], v3, s[4:7], s47 offen nt
	ds_write_b128 v5, v[12:15] offset:768
	ds_write_b128 v5, v[16:19] offset:2816
	s_waitcnt lgkmcnt(0)
	s_barrier
	ds_read_b128 v[12:15], v6 offset:0
	ds_read_b128 v[16:19], v6 offset:2048
	ds_read_b128 v[20:23], v7 offset:0
	ds_read_b128 v[24:27], v7 offset:2048
	ds_read_b128 v[28:31], v8 offset:0
	ds_read_b128 v[32:35], v8 offset:2048
	ds_read_b128 v[36:39], v9 offset:0
	ds_read_b128 v[40:43], v9 offset:2048
	s_waitcnt vmcnt(32)
	s_waitcnt lgkmcnt(7)
	v_mfma_f32_16x16x32_f16 v[188:191], v[108:111], v[12:15], 0
	v_mfma_f32_16x16x32_f16 v[220:223], v[148:151], v[12:15], 0
	s_waitcnt lgkmcnt(6)
	v_mfma_f32_16x16x32_f16 v[192:195], v[112:115], v[16:19], 0
	v_mfma_f32_16x16x32_f16 v[224:227], v[152:155], v[16:19], 0
	s_waitcnt lgkmcnt(5)
	v_mfma_f32_16x16x32_f16 v[196:199], v[116:119], v[20:23], 0
	v_mfma_f32_16x16x32_f16 v[228:231], v[156:159], v[20:23], 0
	s_waitcnt lgkmcnt(4)
	v_mfma_f32_16x16x32_f16 v[200:203], v[120:123], v[24:27], 0
	v_mfma_f32_16x16x32_f16 v[232:235], v[160:163], v[24:27], 0
	s_waitcnt lgkmcnt(3)
	v_mfma_f32_16x16x32_f16 v[204:207], v[124:127], v[28:31], 0
	v_mfma_f32_16x16x32_f16 v[236:239], v[164:167], v[28:31], 0
	s_waitcnt lgkmcnt(2)
	v_mfma_f32_16x16x32_f16 v[208:211], v[128:131], v[32:35], 0
	v_mfma_f32_16x16x32_f16 v[240:243], v[168:171], v[32:35], 0
	s_waitcnt lgkmcnt(1)
	v_mfma_f32_16x16x32_f16 v[212:215], v[132:135], v[36:39], 0
	v_mfma_f32_16x16x32_f16 v[244:247], v[172:175], v[36:39], 0
	s_waitcnt lgkmcnt(0)
	v_mfma_f32_16x16x32_f16 v[216:219], v[136:139], v[40:43], 0
	v_mfma_f32_16x16x32_f16 v[248:251], v[176:179], v[40:43], 0
	s_waitcnt vmcnt(24)
	v_cvt_pkrtz_f16_f32 v12, v44, v46
	v_cvt_pkrtz_f16_f32 v13, v48, v50
	v_cvt_pkrtz_f16_f32 v14, v52, v54
	v_cvt_pkrtz_f16_f32 v15, v56, v58
	v_cvt_pkrtz_f16_f32 v16, v45, v47
	v_cvt_pkrtz_f16_f32 v17, v49, v51
	v_cvt_pkrtz_f16_f32 v18, v53, v55
	v_cvt_pkrtz_f16_f32 v19, v57, v59
.Lpace_4:
	s_memrealtime s[54:55]
	s_waitcnt lgkmcnt(0)
	s_sub_u32 s54, s54, s52
	s_cmp_ge_u32 s54, 820
	s_cbranch_scc1 .Lgo_4
	s_sleep 2
	s_branch .Lpace_4
.Lgo_4:
	s_mov_b32 s40, 0x7820
	s_mov_b32 s41, 0x294b0
	s_mov_b32 s42, 0x4b140
	s_mov_b32 s43, 0x6cdd0
	s_mov_b32 s44, 0x8ea60
	s_mov_b32 s45, 0xb06f0
	s_mov_b32 s46, 0xd2380
	s_mov_b32 s47, 0xf4010
	buffer_load_dwordx2 v[44:45], v3, s[4:7], s40 offen nt
	buffer_load_dwordx2 v[46:47], v3, s[4:7], s41 offen nt
	buffer_load_dwordx2 v[48:49], v3, s[4:7], s42 offen nt
	buffer_load_dwordx2 v[50:51], v3, s[4:7], s43 offen nt
	buffer_load_dwordx2 v[52:53], v3, s[4:7], s44 offen nt
	buffer_load_dwordx2 v[54:55], v3, s[4:7], s45 offen nt
	buffer_load_dwordx2 v[56:57], v3, s[4:7], s46 offen nt
	buffer_load_dwordx2 v[58:59], v3, s[4:7], s47 offen nt
	ds_write_b128 v5, v[12:15] offset:1024
	ds_write_b128 v5, v[16:19] offset:3072
	s_waitcnt vmcnt(24)
	v_cvt_pkrtz_f16_f32 v12, v60, v62
	v_cvt_pkrtz_f16_f32 v13, v64, v66
	v_cvt_pkrtz_f16_f32 v14, v68, v70
	v_cvt_pkrtz_f16_f32 v15, v72, v74
	v_cvt_pkrtz_f16_f32 v16, v61, v63
	v_cvt_pkrtz_f16_f32 v17, v65, v67
	v_cvt_pkrtz_f16_f32 v18, v69, v71
	v_cvt_pkrtz_f16_f32 v19, v73, v75
.Lpace_5:
	s_memrealtime s[54:55]
	s_waitcnt lgkmcnt(0)
	s_sub_u32 s54, s54, s52
	s_cmp_ge_u32 s54, 955
	s_cbranch_scc1 .Lgo_5
	s_sleep 2
	s_branch .Lpace_5
.Lgo_5:
	s_mov_b32 s40, 0x115ca0
	s_mov_b32 s41, 0x137930
	s_mov_b32 s42, 0x1595c0
	s_mov_b32 s43, 0x17b250
	s_mov_b32 s44, 0x19cee0
	s_mov_b32 s45, 0x1beb70
	s_mov_b32 s46, 0x1e0800
	s_mov_b32 s47, 0x202490
	buffer_load_dwordx2 v[60:61], v3, s[4:7], s40 offen nt
	buffer_load_dwordx2 v[62:63], v3, s[4:7], s41 offen nt
	buffer_load_dwordx2 v[64:65], v3, s[4:7], s42 offen nt
	buffer_load_dwordx2 v[66:67], v3, s[4:7], s43 offen nt
	buffer_load_dwordx2 v[68:69], v3, s[4:7], s44 offen nt
	buffer_load_dwordx2 v[70:71], v3, s[4:7], s45 offen nt
	buffer_load_dwordx2 v[72:73], v3, s[4:7], s46 offen nt
	buffer_load_dwordx2 v[74:75], v3, s[4:7], s47 offen nt
	ds_write_b128 v5, v[12:15] offset:1280
	ds_write_b128 v5, v[16:19] offset:3328
	s_waitcnt vmcnt(24)
	v_cvt_pkrtz_f16_f32 v12, v76, v78
	v_cvt_pkrtz_f16_f32 v13, v80, v82
	v_cvt_pkrtz_f16_f32 v14, v84, v86
	v_cvt_pkrtz_f16_f32 v15, v88, v90
	v_cvt_pkrtz_f16_f32 v16, v77, v79
	v_cvt_pkrtz_f16_f32 v17, v81, v83
	v_cvt_pkrtz_f16_f32 v18, v85, v87
	v_cvt_pkrtz_f16_f32 v19, v89, v91
.Lpace_6:
	s_memrealtime s[54:55]
	s_waitcnt lgkmcnt(0)
	s_sub_u32 s54, s54, s52
	s_cmp_ge_u32 s54, 1090
	s_cbranch_scc1 .Lgo_6
	s_sleep 2
	s_branch .Lpace_6
.Lgo_6:
	s_mov_b32 s40, 0x224120
	s_mov_b32 s41, 0x245db0
	s_mov_b32 s42, 0x267a40
	s_mov_b32 s43, 0x2896d0
	s_mov_b32 s44, 0x2ab360
	s_mov_b32 s45, 0x2ccff0
	s_mov_b32 s46, 0x2eec80
	s_mov_b32 s47, 0x310910
	buffer_load_dwordx2 v[76:77], v3, s[4:7], s40 offen nt
	buffer_load_dwordx2 v[78:79], v3, s[4:7], s41 offen nt
	buffer_load_dwordx2 v[80:81], v3, s[4:7], s42 offen nt
	buffer_load_dwordx2 v[82:83], v3, s[4:7], s43 offen nt
	buffer_load_dwordx2 v[84:85], v3, s[4:7], s44 offen nt
	buffer_load_dwordx2 v[86:87], v3, s[4:7], s45 offen nt
	buffer_load_dwordx2 v[88:89], v3, s[4:7], s46 offen nt
	buffer_load_dwordx2 v[90:91], v3, s[4:7], s47 offen nt
	ds_write_b128 v5, v[12:15] offset:1536
	ds_write_b128 v5, v[16:19] offset:3584
	s_waitcnt vmcnt(24)
	v_cvt_pkrtz_f16_f32 v12, v92, v94
	v_cvt_pkrtz_f16_f32 v13, v96, v98
	v_cvt_pkrtz_f16_f32 v14, v100, v102
	v_cvt_pkrtz_f16_f32 v15, v104, v106
	v_cvt_pkrtz_f16_f32 v16, v93, v95
	v_cvt_pkrtz_f16_f32 v17, v97, v99
	v_cvt_pkrtz_f16_f32 v18, v101, v103
	v_cvt_pkrtz_f16_f32 v19, v105, v107
.Lpace_7:
	s_memrealtime s[54:55]
	s_waitcnt lgkmcnt(0)
	s_sub_u32 s54, s54, s52
	s_cmp_ge_u32 s54, 1225
	s_cbranch_scc1 .Lgo_7
	s_sleep 2
	s_branch .Lpace_7
.Lgo_7:
	s_mov_b32 s40, 0x3325a0
	s_mov_b32 s41, 0x354230
	s_mov_b32 s42, 0x375ec0
	s_mov_b32 s43, 0x397b50
	s_mov_b32 s44, 0x3b97e0
	s_mov_b32 s45, 0x3db470
	s_mov_b32 s46, 0x3fd100
	s_mov_b32 s47, 0x41ed90
	buffer_load_dwordx2 v[92:93], v3, s[4:7], s40 offen nt
	buffer_load_dwordx2 v[94:95], v3, s[4:7], s41 offen nt
	buffer_load_dwordx2 v[96:97], v3, s[4:7], s42 offen nt
	buffer_load_dwordx2 v[98:99], v3, s[4:7], s43 offen nt
	buffer_load_dwordx2 v[100:101], v3, s[4:7], s44 offen nt
	buffer_load_dwordx2 v[102:103], v3, s[4:7], s45 offen nt
	buffer_load_dwordx2 v[104:105], v3, s[4:7], s46 offen nt
	buffer_load_dwordx2 v[106:107], v3, s[4:7], s47 offen nt
	ds_write_b128 v5, v[12:15] offset:1792
	ds_write_b128 v5, v[16:19] offset:3840
	s_waitcnt lgkmcnt(0)
	s_barrier
	ds_read_b128 v[12:15], v6 offset:1024
	ds_read_b128 v[16:19], v6 offset:3072
	ds_read_b128 v[20:23], v7 offset:1024
	ds_read_b128 v[24:27], v7 offset:3072
	ds_read_b128 v[28:31], v8 offset:1024
	ds_read_b128 v[32:35], v8 offset:3072
	ds_read_b128 v[36:39], v9 offset:1024
	ds_read_b128 v[40:43], v9 offset:3072
	s_waitcnt lgkmcnt(7)
	v_mfma_f32_16x16x32_f16 v[188:191], v[112:115], v[12:15], v[188:191]
	v_mfma_f32_16x16x32_f16 v[220:223], v[152:155], v[12:15], v[220:223]
	s_waitcnt lgkmcnt(6)
	v_mfma_f32_16x16x32_f16 v[192:195], v[116:119], v[16:19], v[192:195]
	v_mfma_f32_16x16x32_f16 v[224:227], v[156:159], v[16:19], v[224:227]
	s_waitcnt lgkmcnt(5)
	v_mfma_f32_16x16x32_f16 v[196:199], v[120:123], v[20:23], v[196:199]
	v_mfma_f32_16x16x32_f16 v[228:231], v[160:163], v[20:23], v[228:231]
	s_waitcnt lgkmcnt(4)
	v_mfma_f32_16x16x32_f16 v[200:203], v[124:127], v[24:27], v[200:203]
	v_mfma_f32_16x16x32_f16 v[232:235], v[164:167], v[24:27], v[232:235]
	s_waitcnt lgkmcnt(3)
	v_mfma_f32_16x16x32_f16 v[204:207], v[128:131], v[28:31], v[204:207]
	v_mfma_f32_16x16x32_f16 v[236:239], v[168:171], v[28:31], v[236:239]
	s_waitcnt lgkmcnt(2)
	v_mfma_f32_16x16x32_f16 v[208:211], v[132:135], v[32:35], v[208:211]
	v_mfma_f32_16x16x32_f16 v[240:243], v[172:175], v[32:35], v[240:243]
	s_waitcnt lgkmcnt(1)
	v_mfma_f32_16x16x32_f16 v[212:215], v[136:139], v[36:39], v[212:215]
	v_mfma_f32_16x16x32_f16 v[244:247], v[176:179], v[36:39], v[244:247]
	s_waitcnt lgkmcnt(0)
	v_mfma_f32_16x16x32_f16 v[216:219], v[140:143], v[40:43], v[216:219]
	v_mfma_f32_16x16x32_f16 v[248:251], v[180:183], v[40:43], v[248:251]
	s_waitcnt vmcnt(24)
	v_cvt_pkrtz_f16_f32 v12, v44, v46
	v_cvt_pkrtz_f16_f32 v13, v48, v50
	v_cvt_pkrtz_f16_f32 v14, v52, v54
	v_cvt_pkrtz_f16_f32 v15, v56, v58
	v_cvt_pkrtz_f16_f32 v16, v45, v47
	v_cvt_pkrtz_f16_f32 v17, v49, v51
	v_cvt_pkrtz_f16_f32 v18, v53, v55
	v_cvt_pkrtz_f16_f32 v19, v57, v59
.Lpace_8:
	s_memrealtime s[54:55]
	s_waitcnt lgkmcnt(0)
	s_sub_u32 s54, s54, s52
	s_cmp_ge_u32 s54, 1360
	s_cbranch_scc1 .Lgo_8
	s_sleep 2
	s_branch .Lpace_8
.Lgo_8:
	s_mov_b32 s40, 0xb430
	s_mov_b32 s41, 0x2d0c0
	s_mov_b32 s42, 0x4ed50
	s_mov_b32 s43, 0x709e0
	s_mov_b32 s44, 0x92670
	s_mov_b32 s45, 0xb4300
	s_mov_b32 s46, 0xd5f90
	s_mov_b32 s47, 0xf7c20
	buffer_load_dwordx2 v[44:45], v3, s[4:7], s40 offen nt
	buffer_load_dwordx2 v[46:47], v3, s[4:7], s41 offen nt
	buffer_load_dwordx2 v[48:49], v3, s[4:7], s42 offen nt
	buffer_load_dwordx2 v[50:51], v3, s[4:7], s43 offen nt
	buffer_load_dwordx2 v[52:53], v3, s[4:7], s44 offen nt
	buffer_load_dwordx2 v[54:55], v3, s[4:7], s45 offen nt
	buffer_load_dwordx2 v[56:57], v3, s[4:7], s46 offen nt
	buffer_load_dwordx2 v[58:59], v3, s[4:7], s47 offen nt
	ds_write_b128 v5, v[12:15] offset:0
	ds_write_b128 v5, v[16:19] offset:2048
	s_waitcnt vmcnt(24)
	v_cvt_pkrtz_f16_f32 v12, v60, v62
	v_cvt_pkrtz_f16_f32 v13, v64, v66
	v_cvt_pkrtz_f16_f32 v14, v68, v70
	v_cvt_pkrtz_f16_f32 v15, v72, v74
	v_cvt_pkrtz_f16_f32 v16, v61, v63
	v_cvt_pkrtz_f16_f32 v17, v65, v67
	v_cvt_pkrtz_f16_f32 v18, v69, v71
	v_cvt_pkrtz_f16_f32 v19, v73, v75
.Lpace_9:
	s_memrealtime s[54:55]
	s_waitcnt lgkmcnt(0)
	s_sub_u32 s54, s54, s52
	s_cmp_ge_u32 s54, 1495
	s_cbranch_scc1 .Lgo_9
	s_sleep 2
	s_branch .Lpace_9
.Lgo_9:
	s_mov_b32 s40, 0x1198b0
	s_mov_b32 s41, 0x13b540
	s_mov_b32 s42, 0x15d1d0
	s_mov_b32 s43, 0x17ee60
	s_mov_b32 s44, 0x1a0af0
	s_mov_b32 s45, 0x1c2780
	s_mov_b32 s46, 0x1e4410
	s_mov_b32 s47, 0x2060a0
	buffer_load_dwordx2 v[60:61], v3, s[4:7], s40 offen nt
	buffer_load_dwordx2 v[62:63], v3, s[4:7], s41 offen nt
	buffer_load_dwordx2 v[64:65], v3, s[4:7], s42 offen nt
	buffer_load_dwordx2 v[66:67], v3, s[4:7], s43 offen nt
	buffer_load_dwordx2 v[68:69], v3, s[4:7], s44 offen nt
	buffer_load_dwordx2 v[70:71], v3, s[4:7], s45 offen nt
	buffer_load_dwordx2 v[72:73], v3, s[4:7], s46 offen nt
	buffer_load_dwordx2 v[74:75], v3, s[4:7], s47 offen nt
	ds_write_b128 v5, v[12:15] offset:256
	ds_write_b128 v5, v[16:19] offset:2304
	s_waitcnt vmcnt(24)
	v_cvt_pkrtz_f16_f32 v12, v76, v78
	v_cvt_pkrtz_f16_f32 v13, v80, v82
	v_cvt_pkrtz_f16_f32 v14, v84, v86
	v_cvt_pkrtz_f16_f32 v15, v88, v90
	v_cvt_pkrtz_f16_f32 v16, v77, v79
	v_cvt_pkrtz_f16_f32 v17, v81, v83
	v_cvt_pkrtz_f16_f32 v18, v85, v87
	v_cvt_pkrtz_f16_f32 v19, v89, v91
.Lpace_10:
	s_memrealtime s[54:55]
	s_waitcnt lgkmcnt(0)
	s_sub_u32 s54, s54, s52
	s_cmp_ge_u32 s54, 1630
	s_cbranch_scc1 .Lgo_10
	s_sleep 2
	s_branch .Lpace_10
.Lgo_10:
	s_mov_b32 s40, 0x227d30
	s_mov_b32 s41, 0x2499c0
	s_mov_b32 s42, 0x26b650
	s_mov_b32 s43, 0x28d2e0
	s_mov_b32 s44, 0x2aef70
	s_mov_b32 s45, 0x2d0c00
	s_mov_b32 s46, 0x2f2890
	s_mov_b32 s47, 0x314520
	buffer_load_dwordx2 v[76:77], v3, s[4:7], s40 offen nt
	buffer_load_dwordx2 v[78:79], v3, s[4:7], s41 offen nt
	buffer_load_dwordx2 v[80:81], v3, s[4:7], s42 offen nt
	buffer_load_dwordx2 v[82:83], v3, s[4:7], s43 offen nt
	buffer_load_dwordx2 v[84:85], v3, s[4:7], s44 offen nt
	buffer_load_dwordx2 v[86:87], v3, s[4:7], s45 offen nt
	buffer_load_dwordx2 v[88:89], v3, s[4:7], s46 offen nt
	buffer_load_dwordx2 v[90:91], v3, s[4:7], s47 offen nt
	ds_write_b128 v5, v[12:15] offset:512
	ds_write_b128 v5, v[16:19] offset:2560
	s_waitcnt vmcnt(24)
	v_cvt_pkrtz_f16_f32 v12, v92, v94
	v_cvt_pkrtz_f16_f32 v13, v96, v98
	v_cvt_pkrtz_f16_f32 v14, v100, v102
	v_cvt_pkrtz_f16_f32 v15, v104, v106
	v_cvt_pkrtz_f16_f32 v16, v93, v95
	v_cvt_pkrtz_f16_f32 v17, v97, v99
	v_cvt_pkrtz_f16_f32 v18, v101, v103
	v_cvt_pkrtz_f16_f32 v19, v105, v107
.Lpace_11:
	s_memrealtime s[54:55]
	s_waitcnt lgkmcnt(0)
	s_sub_u32 s54, s54, s52
	s_cmp_ge_u32 s54, 1765
	s_cbranch_scc1 .Lgo_11
	s_sleep 2
	s_branch .Lpace_11
.Lgo_11:
	s_mov_b32 s40, 0x3361b0
	s_mov_b32 s41, 0x357e40
	s_mov_b32 s42, 0x379ad0
	s_mov_b32 s43, 0x39b760
	s_mov_b32 s44, 0x3bd3f0
	s_mov_b32 s45, 0x3df080
	s_mov_b32 s46, 0x400d10
	s_mov_b32 s47, 0x4229a0
	buffer_load_dwordx2 v[92:93], v3, s[4:7], s40 offen nt
	buffer_load_dwordx2 v[94:95], v3, s[4:7], s41 offen nt
	buffer_load_dwordx2 v[96:97], v3, s[4:7], s42 offen nt
	buffer_load_dwordx2 v[98:99], v3, s[4:7], s43 offen nt
	buffer_load_dwordx2 v[100:101], v3, s[4:7], s44 offen nt
	buffer_load_dwordx2 v[102:103], v3, s[4:7], s45 offen nt
	buffer_load_dwordx2 v[104:105], v3, s[4:7], s46 offen nt
	buffer_load_dwordx2 v[106:107], v3, s[4:7], s47 offen nt
	ds_write_b128 v5, v[12:15] offset:768
	ds_write_b128 v5, v[16:19] offset:2816
	s_waitcnt lgkmcnt(0)
	s_barrier
	ds_read_b128 v[12:15], v6 offset:0
	ds_read_b128 v[16:19], v6 offset:2048
	ds_read_b128 v[20:23], v7 offset:0
	ds_read_b128 v[24:27], v7 offset:2048
	ds_read_b128 v[28:31], v8 offset:0
	ds_read_b128 v[32:35], v8 offset:2048
	ds_read_b128 v[36:39], v9 offset:0
	ds_read_b128 v[40:43], v9 offset:2048
	s_waitcnt lgkmcnt(7)
	v_mfma_f32_16x16x32_f16 v[188:191], v[116:119], v[12:15], v[188:191]
	v_mfma_f32_16x16x32_f16 v[220:223], v[156:159], v[12:15], v[220:223]
	s_waitcnt lgkmcnt(6)
	v_mfma_f32_16x16x32_f16 v[192:195], v[120:123], v[16:19], v[192:195]
	v_mfma_f32_16x16x32_f16 v[224:227], v[160:163], v[16:19], v[224:227]
	s_waitcnt lgkmcnt(5)
	v_mfma_f32_16x16x32_f16 v[196:199], v[124:127], v[20:23], v[196:199]
	v_mfma_f32_16x16x32_f16 v[228:231], v[164:167], v[20:23], v[228:231]
	s_waitcnt lgkmcnt(4)
	v_mfma_f32_16x16x32_f16 v[200:203], v[128:131], v[24:27], v[200:203]
	v_mfma_f32_16x16x32_f16 v[232:235], v[168:171], v[24:27], v[232:235]
	s_waitcnt lgkmcnt(3)
	v_mfma_f32_16x16x32_f16 v[204:207], v[132:135], v[28:31], v[204:207]
	v_mfma_f32_16x16x32_f16 v[236:239], v[172:175], v[28:31], v[236:239]
	s_waitcnt lgkmcnt(2)
	v_mfma_f32_16x16x32_f16 v[208:211], v[136:139], v[32:35], v[208:211]
	v_mfma_f32_16x16x32_f16 v[240:243], v[176:179], v[32:35], v[240:243]
	s_waitcnt lgkmcnt(1)
	v_mfma_f32_16x16x32_f16 v[212:215], v[140:143], v[36:39], v[212:215]
	v_mfma_f32_16x16x32_f16 v[244:247], v[180:183], v[36:39], v[244:247]
	s_waitcnt lgkmcnt(0)
	v_mfma_f32_16x16x32_f16 v[216:219], v[144:147], v[40:43], v[216:219]
	v_mfma_f32_16x16x32_f16 v[248:251], v[184:187], v[40:43], v[248:251]
	s_mov_b32 s40, 0x20000
	s_mov_b32 s41, 0x20400
	s_mov_b32 s42, 0x20800
	s_mov_b32 s43, 0x20c00
	s_mov_b32 s44, 0x21000
	buffer_load_dwordx4 v[108:111], v4, s[8:11], s40 offen
	buffer_load_dwordx4 v[112:115], v4, s[8:11], s41 offen
	buffer_load_dwordx4 v[116:119], v4, s[8:11], s42 offen
	buffer_load_dwordx4 v[120:123], v4, s[8:11], s43 offen
	buffer_load_dwordx4 v[124:127], v4, s[8:11], s44 offen
	s_mov_b32 s40, 0x21400
	s_mov_b32 s41, 0x21800
	s_mov_b32 s42, 0x21c00
	s_mov_b32 s43, 0x22000
	s_mov_b32 s44, 0x22400
	buffer_load_dwordx4 v[128:131], v4, s[8:11], s40 offen
	buffer_load_dwordx4 v[132:135], v4, s[8:11], s41 offen
	buffer_load_dwordx4 v[136:139], v4, s[8:11], s42 offen
	buffer_load_dwordx4 v[140:143], v4, s[8:11], s43 offen
	buffer_load_dwordx4 v[144:147], v4, s[8:11], s44 offen
	s_waitcnt vmcnt(34)
	v_cvt_pkrtz_f16_f32 v12, v44, v46
	v_cvt_pkrtz_f16_f32 v13, v48, v50
	v_cvt_pkrtz_f16_f32 v14, v52, v54
	v_cvt_pkrtz_f16_f32 v15, v56, v58
	v_cvt_pkrtz_f16_f32 v16, v45, v47
	v_cvt_pkrtz_f16_f32 v17, v49, v51
	v_cvt_pkrtz_f16_f32 v18, v53, v55
	v_cvt_pkrtz_f16_f32 v19, v57, v59
.Lpace_12:
	s_memrealtime s[54:55]
	s_waitcnt lgkmcnt(0)
	s_sub_u32 s54, s54, s52
	s_cmp_ge_u32 s54, 1900
	s_cbranch_scc1 .Lgo_12
	s_sleep 2
	s_branch .Lpace_12
.Lgo_12:
	s_mov_b32 s40, 0xf040
	s_mov_b32 s41, 0x30cd0
	s_mov_b32 s42, 0x52960
	s_mov_b32 s43, 0x745f0
	s_mov_b32 s44, 0x96280
	s_mov_b32 s45, 0xb7f10
	s_mov_b32 s46, 0xd9ba0
	s_mov_b32 s47, 0xfb830
	buffer_load_dwordx2 v[44:45], v3, s[4:7], s40 offen nt
	buffer_load_dwordx2 v[46:47], v3, s[4:7], s41 offen nt
	buffer_load_dwordx2 v[48:49], v3, s[4:7], s42 offen nt
	buffer_load_dwordx2 v[50:51], v3, s[4:7], s43 offen nt
	buffer_load_dwordx2 v[52:53], v3, s[4:7], s44 offen nt
	buffer_load_dwordx2 v[54:55], v3, s[4:7], s45 offen nt
	buffer_load_dwordx2 v[56:57], v3, s[4:7], s46 offen nt
	buffer_load_dwordx2 v[58:59], v3, s[4:7], s47 offen nt
	ds_write_b128 v5, v[12:15] offset:1024
	ds_write_b128 v5, v[16:19] offset:3072
	s_waitcnt vmcnt(34)
	v_cvt_pkrtz_f16_f32 v12, v60, v62
	v_cvt_pkrtz_f16_f32 v13, v64, v66
	v_cvt_pkrtz_f16_f32 v14, v68, v70
	v_cvt_pkrtz_f16_f32 v15, v72, v74
	v_cvt_pkrtz_f16_f32 v16, v61, v63
	v_cvt_pkrtz_f16_f32 v17, v65, v67
	v_cvt_pkrtz_f16_f32 v18, v69, v71
	v_cvt_pkrtz_f16_f32 v19, v73, v75
.Lpace_13:
	s_memrealtime s[54:55]
	s_waitcnt lgkmcnt(0)
	s_sub_u32 s54, s54, s52
	s_cmp_ge_u32 s54, 2035
	s_cbranch_scc1 .Lgo_13
	s_sleep 2
	s_branch .Lpace_13
.Lgo_13:
	s_mov_b32 s40, 0x11d4c0
	s_mov_b32 s41, 0x13f150
	s_mov_b32 s42, 0x160de0
	s_mov_b32 s43, 0x182a70
	s_mov_b32 s44, 0x1a4700
	s_mov_b32 s45, 0x1c6390
	s_mov_b32 s46, 0x1e8020
	s_mov_b32 s47, 0x209cb0
	buffer_load_dwordx2 v[60:61], v3, s[4:7], s40 offen nt
	buffer_load_dwordx2 v[62:63], v3, s[4:7], s41 offen nt
	buffer_load_dwordx2 v[64:65], v3, s[4:7], s42 offen nt
	buffer_load_dwordx2 v[66:67], v3, s[4:7], s43 offen nt
	buffer_load_dwordx2 v[68:69], v3, s[4:7], s44 offen nt
	buffer_load_dwordx2 v[70:71], v3, s[4:7], s45 offen nt
	buffer_load_dwordx2 v[72:73], v3, s[4:7], s46 offen nt
	buffer_load_dwordx2 v[74:75], v3, s[4:7], s47 offen nt
	ds_write_b128 v5, v[12:15] offset:1280
	ds_write_b128 v5, v[16:19] offset:3328
	s_waitcnt vmcnt(34)
	v_cvt_pkrtz_f16_f32 v12, v76, v78
	v_cvt_pkrtz_f16_f32 v13, v80, v82
	v_cvt_pkrtz_f16_f32 v14, v84, v86
	v_cvt_pkrtz_f16_f32 v15, v88, v90
	v_cvt_pkrtz_f16_f32 v16, v77, v79
	v_cvt_pkrtz_f16_f32 v17, v81, v83
	v_cvt_pkrtz_f16_f32 v18, v85, v87
	v_cvt_pkrtz_f16_f32 v19, v89, v91
.Lpace_14:
	s_memrealtime s[54:55]
	s_waitcnt lgkmcnt(0)
	s_sub_u32 s54, s54, s52
	s_cmp_ge_u32 s54, 2170
	s_cbranch_scc1 .Lgo_14
	s_sleep 2
	s_branch .Lpace_14
.Lgo_14:
	s_mov_b32 s40, 0x22b940
	s_mov_b32 s41, 0x24d5d0
	s_mov_b32 s42, 0x26f260
	s_mov_b32 s43, 0x290ef0
	s_mov_b32 s44, 0x2b2b80
	s_mov_b32 s45, 0x2d4810
	s_mov_b32 s46, 0x2f64a0
	s_mov_b32 s47, 0x318130
	buffer_load_dwordx2 v[76:77], v3, s[4:7], s40 offen nt
	buffer_load_dwordx2 v[78:79], v3, s[4:7], s41 offen nt
	buffer_load_dwordx2 v[80:81], v3, s[4:7], s42 offen nt
	buffer_load_dwordx2 v[82:83], v3, s[4:7], s43 offen nt
	buffer_load_dwordx2 v[84:85], v3, s[4:7], s44 offen nt
	buffer_load_dwordx2 v[86:87], v3, s[4:7], s45 offen nt
	buffer_load_dwordx2 v[88:89], v3, s[4:7], s46 offen nt
	buffer_load_dwordx2 v[90:91], v3, s[4:7], s47 offen nt
	ds_write_b128 v5, v[12:15] offset:1536
	ds_write_b128 v5, v[16:19] offset:3584
	s_waitcnt vmcnt(34)
	v_cvt_pkrtz_f16_f32 v12, v92, v94
	v_cvt_pkrtz_f16_f32 v13, v96, v98
	v_cvt_pkrtz_f16_f32 v14, v100, v102
	v_cvt_pkrtz_f16_f32 v15, v104, v106
	v_cvt_pkrtz_f16_f32 v16, v93, v95
	v_cvt_pkrtz_f16_f32 v17, v97, v99
	v_cvt_pkrtz_f16_f32 v18, v101, v103
	v_cvt_pkrtz_f16_f32 v19, v105, v107
.Lpace_15:
	s_memrealtime s[54:55]
	s_waitcnt lgkmcnt(0)
	s_sub_u32 s54, s54, s52
	s_cmp_ge_u32 s54, 2305
	s_cbranch_scc1 .Lgo_15
	s_sleep 2
	s_branch .Lpace_15
.Lgo_15:
	s_mov_b32 s40, 0x339dc0
	s_mov_b32 s41, 0x35ba50
	s_mov_b32 s42, 0x37d6e0
	s_mov_b32 s43, 0x39f370
	s_mov_b32 s44, 0x3c1000
	s_mov_b32 s45, 0x3e2c90
	s_mov_b32 s46, 0x404920
	s_mov_b32 s47, 0x4265b0
	buffer_load_dwordx2 v[92:93], v3, s[4:7], s40 offen nt
	buffer_load_dwordx2 v[94:95], v3, s[4:7], s41 offen nt
	buffer_load_dwordx2 v[96:97], v3, s[4:7], s42 offen nt
	buffer_load_dwordx2 v[98:99], v3, s[4:7], s43 offen nt
	buffer_load_dwordx2 v[100:101], v3, s[4:7], s44 offen nt
	buffer_load_dwordx2 v[102:103], v3, s[4:7], s45 offen nt
	buffer_load_dwordx2 v[104:105], v3, s[4:7], s46 offen nt
	buffer_load_dwordx2 v[106:107], v3, s[4:7], s47 offen nt
	ds_write_b128 v5, v[12:15] offset:1792
	ds_write_b128 v5, v[16:19] offset:3840
	s_waitcnt lgkmcnt(0)
	s_barrier
	ds_read_b128 v[12:15], v6 offset:1024
	ds_read_b128 v[16:19], v6 offset:3072
	ds_read_b128 v[20:23], v7 offset:1024
	ds_read_b128 v[24:27], v7 offset:3072
	ds_read_b128 v[28:31], v8 offset:1024
	ds_read_b128 v[32:35], v8 offset:3072
	ds_read_b128 v[36:39], v9 offset:1024
	ds_read_b128 v[40:43], v9 offset:3072
	s_waitcnt vmcnt(32)
	s_waitcnt lgkmcnt(7)
	v_mfma_f32_16x16x32_f16 v[188:191], v[148:151], v[12:15], v[188:191]
	v_mfma_f32_16x16x32_f16 v[220:223], v[108:111], v[12:15], v[220:223]
	s_waitcnt lgkmcnt(6)
	v_mfma_f32_16x16x32_f16 v[192:195], v[152:155], v[16:19], v[192:195]
	v_mfma_f32_16x16x32_f16 v[224:227], v[112:115], v[16:19], v[224:227]
	s_waitcnt lgkmcnt(5)
	v_mfma_f32_16x16x32_f16 v[196:199], v[156:159], v[20:23], v[196:199]
	v_mfma_f32_16x16x32_f16 v[228:231], v[116:119], v[20:23], v[228:231]
	s_waitcnt lgkmcnt(4)
	v_mfma_f32_16x16x32_f16 v[200:203], v[160:163], v[24:27], v[200:203]
	v_mfma_f32_16x16x32_f16 v[232:235], v[120:123], v[24:27], v[232:235]
	s_waitcnt lgkmcnt(3)
	v_mfma_f32_16x16x32_f16 v[204:207], v[164:167], v[28:31], v[204:207]
	v_mfma_f32_16x16x32_f16 v[236:239], v[124:127], v[28:31], v[236:239]
	s_waitcnt lgkmcnt(2)
	v_mfma_f32_16x16x32_f16 v[208:211], v[168:171], v[32:35], v[208:211]
	v_mfma_f32_16x16x32_f16 v[240:243], v[128:131], v[32:35], v[240:243]
	s_waitcnt lgkmcnt(1)
	v_mfma_f32_16x16x32_f16 v[212:215], v[172:175], v[36:39], v[212:215]
	v_mfma_f32_16x16x32_f16 v[244:247], v[132:135], v[36:39], v[244:247]
	s_waitcnt lgkmcnt(0)
	v_mfma_f32_16x16x32_f16 v[216:219], v[176:179], v[40:43], v[216:219]
	v_mfma_f32_16x16x32_f16 v[248:251], v[136:139], v[40:43], v[248:251]
	s_waitcnt vmcnt(24)
	v_cvt_pkrtz_f16_f32 v12, v44, v46
	v_cvt_pkrtz_f16_f32 v13, v48, v50
	v_cvt_pkrtz_f16_f32 v14, v52, v54
	v_cvt_pkrtz_f16_f32 v15, v56, v58
	v_cvt_pkrtz_f16_f32 v16, v45, v47
	v_cvt_pkrtz_f16_f32 v17, v49, v51
	v_cvt_pkrtz_f16_f32 v18, v53, v55
	v_cvt_pkrtz_f16_f32 v19, v57, v59
.Lpace_16:
	s_memrealtime s[54:55]
	s_waitcnt lgkmcnt(0)
	s_sub_u32 s54, s54, s52
	s_cmp_ge_u32 s54, 2440
	s_cbranch_scc1 .Lgo_16
	s_sleep 2
	s_branch .Lpace_16
.Lgo_16:
	s_mov_b32 s40, 0x12c50
	s_mov_b32 s41, 0x348e0
	s_mov_b32 s42, 0x56570
	s_mov_b32 s43, 0x78200
	s_mov_b32 s44, 0x99e90
	s_mov_b32 s45, 0xbbb20
	s_mov_b32 s46, 0xdd7b0
	s_mov_b32 s47, 0xff440
	buffer_load_dwordx2 v[44:45], v3, s[4:7], s40 offen nt
	buffer_load_dwordx2 v[46:47], v3, s[4:7], s41 offen nt
	buffer_load_dwordx2 v[48:49], v3, s[4:7], s42 offen nt
	buffer_load_dwordx2 v[50:51], v3, s[4:7], s43 offen nt
	buffer_load_dwordx2 v[52:53], v3, s[4:7], s44 offen nt
	buffer_load_dwordx2 v[54:55], v3, s[4:7], s45 offen nt
	buffer_load_dwordx2 v[56:57], v3, s[4:7], s46 offen nt
	buffer_load_dwordx2 v[58:59], v3, s[4:7], s47 offen nt
	ds_write_b128 v5, v[12:15] offset:0
	ds_write_b128 v5, v[16:19] offset:2048
	s_waitcnt vmcnt(24)
	v_cvt_pkrtz_f16_f32 v12, v60, v62
	v_cvt_pkrtz_f16_f32 v13, v64, v66
	v_cvt_pkrtz_f16_f32 v14, v68, v70
	v_cvt_pkrtz_f16_f32 v15, v72, v74
	v_cvt_pkrtz_f16_f32 v16, v61, v63
	v_cvt_pkrtz_f16_f32 v17, v65, v67
	v_cvt_pkrtz_f16_f32 v18, v69, v71
	v_cvt_pkrtz_f16_f32 v19, v73, v75
.Lpace_17:
	s_memrealtime s[54:55]
	s_waitcnt lgkmcnt(0)
	s_sub_u32 s54, s54, s52
	s_cmp_ge_u32 s54, 2575
	s_cbranch_scc1 .Lgo_17
	s_sleep 2
	s_branch .Lpace_17
.Lgo_17:
	s_mov_b32 s40, 0x1210d0
	s_mov_b32 s41, 0x142d60
	s_mov_b32 s42, 0x1649f0
	s_mov_b32 s43, 0x186680
	s_mov_b32 s44, 0x1a8310
	s_mov_b32 s45, 0x1c9fa0
	s_mov_b32 s46, 0x1ebc30
	s_mov_b32 s47, 0x20d8c0
	buffer_load_dwordx2 v[60:61], v3, s[4:7], s40 offen nt
	buffer_load_dwordx2 v[62:63], v3, s[4:7], s41 offen nt
	buffer_load_dwordx2 v[64:65], v3, s[4:7], s42 offen nt
	buffer_load_dwordx2 v[66:67], v3, s[4:7], s43 offen nt
	buffer_load_dwordx2 v[68:69], v3, s[4:7], s44 offen nt
	buffer_load_dwordx2 v[70:71], v3, s[4:7], s45 offen nt
	buffer_load_dwordx2 v[72:73], v3, s[4:7], s46 offen nt
	buffer_load_dwordx2 v[74:75], v3, s[4:7], s47 offen nt
	ds_write_b128 v5, v[12:15] offset:256
	ds_write_b128 v5, v[16:19] offset:2304
	s_waitcnt vmcnt(24)
	v_cvt_pkrtz_f16_f32 v12, v76, v78
	v_cvt_pkrtz_f16_f32 v13, v80, v82
	v_cvt_pkrtz_f16_f32 v14, v84, v86
	v_cvt_pkrtz_f16_f32 v15, v88, v90
	v_cvt_pkrtz_f16_f32 v16, v77, v79
	v_cvt_pkrtz_f16_f32 v17, v81, v83
	v_cvt_pkrtz_f16_f32 v18, v85, v87
	v_cvt_pkrtz_f16_f32 v19, v89, v91
.Lpace_18:
	s_memrealtime s[54:55]
	s_waitcnt lgkmcnt(0)
	s_sub_u32 s54, s54, s52
	s_cmp_ge_u32 s54, 2710
	s_cbranch_scc1 .Lgo_18
	s_sleep 2
	s_branch .Lpace_18
.Lgo_18:
	s_mov_b32 s40, 0x22f550
	s_mov_b32 s41, 0x2511e0
	s_mov_b32 s42, 0x272e70
	s_mov_b32 s43, 0x294b00
	s_mov_b32 s44, 0x2b6790
	s_mov_b32 s45, 0x2d8420
	s_mov_b32 s46, 0x2fa0b0
	s_mov_b32 s47, 0x31bd40
	buffer_load_dwordx2 v[76:77], v3, s[4:7], s40 offen nt
	buffer_load_dwordx2 v[78:79], v3, s[4:7], s41 offen nt
	buffer_load_dwordx2 v[80:81], v3, s[4:7], s42 offen nt
	buffer_load_dwordx2 v[82:83], v3, s[4:7], s43 offen nt
	buffer_load_dwordx2 v[84:85], v3, s[4:7], s44 offen nt
	buffer_load_dwordx2 v[86:87], v3, s[4:7], s45 offen nt
	buffer_load_dwordx2 v[88:89], v3, s[4:7], s46 offen nt
	buffer_load_dwordx2 v[90:91], v3, s[4:7], s47 offen nt
	ds_write_b128 v5, v[12:15] offset:512
	ds_write_b128 v5, v[16:19] offset:2560
	s_waitcnt vmcnt(24)
	v_cvt_pkrtz_f16_f32 v12, v92, v94
	v_cvt_pkrtz_f16_f32 v13, v96, v98
	v_cvt_pkrtz_f16_f32 v14, v100, v102
	v_cvt_pkrtz_f16_f32 v15, v104, v106
	v_cvt_pkrtz_f16_f32 v16, v93, v95
	v_cvt_pkrtz_f16_f32 v17, v97, v99
	v_cvt_pkrtz_f16_f32 v18, v101, v103
	v_cvt_pkrtz_f16_f32 v19, v105, v107
.Lpace_19:
	s_memrealtime s[54:55]
	s_waitcnt lgkmcnt(0)
	s_sub_u32 s54, s54, s52
	s_cmp_ge_u32 s54, 2845
	s_cbranch_scc1 .Lgo_19
	s_sleep 2
	s_branch .Lpace_19
.Lgo_19:
	s_mov_b32 s40, 0x33d9d0
	s_mov_b32 s41, 0x35f660
	s_mov_b32 s42, 0x3812f0
	s_mov_b32 s43, 0x3a2f80
	s_mov_b32 s44, 0x3c4c10
	s_mov_b32 s45, 0x3e68a0
	s_mov_b32 s46, 0x408530
	s_mov_b32 s47, 0x42a1c0
	buffer_load_dwordx2 v[92:93], v3, s[4:7], s40 offen nt
	buffer_load_dwordx2 v[94:95], v3, s[4:7], s41 offen nt
	buffer_load_dwordx2 v[96:97], v3, s[4:7], s42 offen nt
	buffer_load_dwordx2 v[98:99], v3, s[4:7], s43 offen nt
	buffer_load_dwordx2 v[100:101], v3, s[4:7], s44 offen nt
	buffer_load_dwordx2 v[102:103], v3, s[4:7], s45 offen nt
	buffer_load_dwordx2 v[104:105], v3, s[4:7], s46 offen nt
	buffer_load_dwordx2 v[106:107], v3, s[4:7], s47 offen nt
	ds_write_b128 v5, v[12:15] offset:768
	ds_write_b128 v5, v[16:19] offset:2816
	s_waitcnt lgkmcnt(0)
	s_barrier
	ds_read_b128 v[12:15], v6 offset:0
	ds_read_b128 v[16:19], v6 offset:2048
	ds_read_b128 v[20:23], v7 offset:0
	ds_read_b128 v[24:27], v7 offset:2048
	ds_read_b128 v[28:31], v8 offset:0
	ds_read_b128 v[32:35], v8 offset:2048
	ds_read_b128 v[36:39], v9 offset:0
	ds_read_b128 v[40:43], v9 offset:2048
	s_waitcnt lgkmcnt(7)
	v_mfma_f32_16x16x32_f16 v[188:191], v[152:155], v[12:15], v[188:191]
	v_mfma_f32_16x16x32_f16 v[220:223], v[112:115], v[12:15], v[220:223]
	s_waitcnt lgkmcnt(6)
	v_mfma_f32_16x16x32_f16 v[192:195], v[156:159], v[16:19], v[192:195]
	v_mfma_f32_16x16x32_f16 v[224:227], v[116:119], v[16:19], v[224:227]
	s_waitcnt lgkmcnt(5)
	v_mfma_f32_16x16x32_f16 v[196:199], v[160:163], v[20:23], v[196:199]
	v_mfma_f32_16x16x32_f16 v[228:231], v[120:123], v[20:23], v[228:231]
	s_waitcnt lgkmcnt(4)
	v_mfma_f32_16x16x32_f16 v[200:203], v[164:167], v[24:27], v[200:203]
	v_mfma_f32_16x16x32_f16 v[232:235], v[124:127], v[24:27], v[232:235]
	s_waitcnt lgkmcnt(3)
	v_mfma_f32_16x16x32_f16 v[204:207], v[168:171], v[28:31], v[204:207]
	v_mfma_f32_16x16x32_f16 v[236:239], v[128:131], v[28:31], v[236:239]
	s_waitcnt lgkmcnt(2)
	v_mfma_f32_16x16x32_f16 v[208:211], v[172:175], v[32:35], v[208:211]
	v_mfma_f32_16x16x32_f16 v[240:243], v[132:135], v[32:35], v[240:243]
	s_waitcnt lgkmcnt(1)
	v_mfma_f32_16x16x32_f16 v[212:215], v[176:179], v[36:39], v[212:215]
	v_mfma_f32_16x16x32_f16 v[244:247], v[136:139], v[36:39], v[244:247]
	s_waitcnt lgkmcnt(0)
	v_mfma_f32_16x16x32_f16 v[216:219], v[180:183], v[40:43], v[216:219]
	v_mfma_f32_16x16x32_f16 v[248:251], v[140:143], v[40:43], v[248:251]
	s_waitcnt vmcnt(24)
	v_cvt_pkrtz_f16_f32 v12, v44, v46
	v_cvt_pkrtz_f16_f32 v13, v48, v50
	v_cvt_pkrtz_f16_f32 v14, v52, v54
	v_cvt_pkrtz_f16_f32 v15, v56, v58
	v_cvt_pkrtz_f16_f32 v16, v45, v47
	v_cvt_pkrtz_f16_f32 v17, v49, v51
	v_cvt_pkrtz_f16_f32 v18, v53, v55
	v_cvt_pkrtz_f16_f32 v19, v57, v59
.Lpace_20:
	s_memrealtime s[54:55]
	s_waitcnt lgkmcnt(0)
	s_sub_u32 s54, s54, s52
	s_cmp_ge_u32 s54, 2980
	s_cbranch_scc1 .Lgo_20
	s_sleep 2
	s_branch .Lpace_20
.Lgo_20:
	s_mov_b32 s40, 0x16860
	s_mov_b32 s41, 0x384f0
	s_mov_b32 s42, 0x5a180
	s_mov_b32 s43, 0x7be10
	s_mov_b32 s44, 0x9daa0
	s_mov_b32 s45, 0xbf730
	s_mov_b32 s46, 0xe13c0
	s_mov_b32 s47, 0x103050
	buffer_load_dwordx2 v[44:45], v3, s[4:7], s40 offen nt
	buffer_load_dwordx2 v[46:47], v3, s[4:7], s41 offen nt
	buffer_load_dwordx2 v[48:49], v3, s[4:7], s42 offen nt
	buffer_load_dwordx2 v[50:51], v3, s[4:7], s43 offen nt
	buffer_load_dwordx2 v[52:53], v3, s[4:7], s44 offen nt
	buffer_load_dwordx2 v[54:55], v3, s[4:7], s45 offen nt
	buffer_load_dwordx2 v[56:57], v3, s[4:7], s46 offen nt
	buffer_load_dwordx2 v[58:59], v3, s[4:7], s47 offen nt
	ds_write_b128 v5, v[12:15] offset:1024
	ds_write_b128 v5, v[16:19] offset:3072
	s_waitcnt vmcnt(24)
	v_cvt_pkrtz_f16_f32 v12, v60, v62
	v_cvt_pkrtz_f16_f32 v13, v64, v66
	v_cvt_pkrtz_f16_f32 v14, v68, v70
	v_cvt_pkrtz_f16_f32 v15, v72, v74
	v_cvt_pkrtz_f16_f32 v16, v61, v63
	v_cvt_pkrtz_f16_f32 v17, v65, v67
	v_cvt_pkrtz_f16_f32 v18, v69, v71
	v_cvt_pkrtz_f16_f32 v19, v73, v75
.Lpace_21:
	s_memrealtime s[54:55]
	s_waitcnt lgkmcnt(0)
	s_sub_u32 s54, s54, s52
	s_cmp_ge_u32 s54, 3115
	s_cbranch_scc1 .Lgo_21
	s_sleep 2
	s_branch .Lpace_21
.Lgo_21:
	s_mov_b32 s40, 0x124ce0
	s_mov_b32 s41, 0x146970
	s_mov_b32 s42, 0x168600
	s_mov_b32 s43, 0x18a290
	s_mov_b32 s44, 0x1abf20
	s_mov_b32 s45, 0x1cdbb0
	s_mov_b32 s46, 0x1ef840
	s_mov_b32 s47, 0x2114d0
	buffer_load_dwordx2 v[60:61], v3, s[4:7], s40 offen nt
	buffer_load_dwordx2 v[62:63], v3, s[4:7], s41 offen nt
	buffer_load_dwordx2 v[64:65], v3, s[4:7], s42 offen nt
	buffer_load_dwordx2 v[66:67], v3, s[4:7], s43 offen nt
	buffer_load_dwordx2 v[68:69], v3, s[4:7], s44 offen nt
	buffer_load_dwordx2 v[70:71], v3, s[4:7], s45 offen nt
	buffer_load_dwordx2 v[72:73], v3, s[4:7], s46 offen nt
	buffer_load_dwordx2 v[74:75], v3, s[4:7], s47 offen nt
	ds_write_b128 v5, v[12:15] offset:1280
	ds_write_b128 v5, v[16:19] offset:3328
	s_waitcnt vmcnt(24)
	v_cvt_pkrtz_f16_f32 v12, v76, v78
	v_cvt_pkrtz_f16_f32 v13, v80, v82
	v_cvt_pkrtz_f16_f32 v14, v84, v86
	v_cvt_pkrtz_f16_f32 v15, v88, v90
	v_cvt_pkrtz_f16_f32 v16, v77, v79
	v_cvt_pkrtz_f16_f32 v17, v81, v83
	v_cvt_pkrtz_f16_f32 v18, v85, v87
	v_cvt_pkrtz_f16_f32 v19, v89, v91
.Lpace_22:
	s_memrealtime s[54:55]
	s_waitcnt lgkmcnt(0)
	s_sub_u32 s54, s54, s52
	s_cmp_ge_u32 s54, 3250
	s_cbranch_scc1 .Lgo_22
	s_sleep 2
	s_branch .Lpace_22
.Lgo_22:
	s_mov_b32 s40, 0x233160
	s_mov_b32 s41, 0x254df0
	s_mov_b32 s42, 0x276a80
	s_mov_b32 s43, 0x298710
	s_mov_b32 s44, 0x2ba3a0
	s_mov_b32 s45, 0x2dc030
	s_mov_b32 s46, 0x2fdcc0
	s_mov_b32 s47, 0x31f950
	buffer_load_dwordx2 v[76:77], v3, s[4:7], s40 offen nt
	buffer_load_dwordx2 v[78:79], v3, s[4:7], s41 offen nt
	buffer_load_dwordx2 v[80:81], v3, s[4:7], s42 offen nt
	buffer_load_dwordx2 v[82:83], v3, s[4:7], s43 offen nt
	buffer_load_dwordx2 v[84:85], v3, s[4:7], s44 offen nt
	buffer_load_dwordx2 v[86:87], v3, s[4:7], s45 offen nt
	buffer_load_dwordx2 v[88:89], v3, s[4:7], s46 offen nt
	buffer_load_dwordx2 v[90:91], v3, s[4:7], s47 offen nt
	ds_write_b128 v5, v[12:15] offset:1536
	ds_write_b128 v5, v[16:19] offset:3584
	s_waitcnt vmcnt(24)
	v_cvt_pkrtz_f16_f32 v12, v92, v94
	v_cvt_pkrtz_f16_f32 v13, v96, v98
	v_cvt_pkrtz_f16_f32 v14, v100, v102
	v_cvt_pkrtz_f16_f32 v15, v104, v106
	v_cvt_pkrtz_f16_f32 v16, v93, v95
	v_cvt_pkrtz_f16_f32 v17, v97, v99
	v_cvt_pkrtz_f16_f32 v18, v101, v103
	v_cvt_pkrtz_f16_f32 v19, v105, v107
.Lpace_23:
	s_memrealtime s[54:55]
	s_waitcnt lgkmcnt(0)
	s_sub_u32 s54, s54, s52
	s_cmp_ge_u32 s54, 3385
	s_cbranch_scc1 .Lgo_23
	s_sleep 2
	s_branch .Lpace_23
.Lgo_23:
	s_mov_b32 s40, 0x3415e0
	s_mov_b32 s41, 0x363270
	s_mov_b32 s42, 0x384f00
	s_mov_b32 s43, 0x3a6b90
	s_mov_b32 s44, 0x3c8820
	s_mov_b32 s45, 0x3ea4b0
	s_mov_b32 s46, 0x40c140
	s_mov_b32 s47, 0x42ddd0
	buffer_load_dwordx2 v[92:93], v3, s[4:7], s40 offen nt
	buffer_load_dwordx2 v[94:95], v3, s[4:7], s41 offen nt
	buffer_load_dwordx2 v[96:97], v3, s[4:7], s42 offen nt
	buffer_load_dwordx2 v[98:99], v3, s[4:7], s43 offen nt
	buffer_load_dwordx2 v[100:101], v3, s[4:7], s44 offen nt
	buffer_load_dwordx2 v[102:103], v3, s[4:7], s45 offen nt
	buffer_load_dwordx2 v[104:105], v3, s[4:7], s46 offen nt
	buffer_load_dwordx2 v[106:107], v3, s[4:7], s47 offen nt
	ds_write_b128 v5, v[12:15] offset:1792
	ds_write_b128 v5, v[16:19] offset:3840
	s_waitcnt lgkmcnt(0)
	s_barrier
	ds_read_b128 v[12:15], v6 offset:1024
	ds_read_b128 v[16:19], v6 offset:3072
	ds_read_b128 v[20:23], v7 offset:1024
	ds_read_b128 v[24:27], v7 offset:3072
	ds_read_b128 v[28:31], v8 offset:1024
	ds_read_b128 v[32:35], v8 offset:3072
	ds_read_b128 v[36:39], v9 offset:1024
	ds_read_b128 v[40:43], v9 offset:3072
	s_waitcnt lgkmcnt(7)
	v_mfma_f32_16x16x32_f16 v[188:191], v[156:159], v[12:15], v[188:191]
	v_mfma_f32_16x16x32_f16 v[220:223], v[116:119], v[12:15], v[220:223]
	s_waitcnt lgkmcnt(6)
	v_mfma_f32_16x16x32_f16 v[192:195], v[160:163], v[16:19], v[192:195]
	v_mfma_f32_16x16x32_f16 v[224:227], v[120:123], v[16:19], v[224:227]
	s_waitcnt lgkmcnt(5)
	v_mfma_f32_16x16x32_f16 v[196:199], v[164:167], v[20:23], v[196:199]
	v_mfma_f32_16x16x32_f16 v[228:231], v[124:127], v[20:23], v[228:231]
	s_waitcnt lgkmcnt(4)
	v_mfma_f32_16x16x32_f16 v[200:203], v[168:171], v[24:27], v[200:203]
	v_mfma_f32_16x16x32_f16 v[232:235], v[128:131], v[24:27], v[232:235]
	s_waitcnt lgkmcnt(3)
	v_mfma_f32_16x16x32_f16 v[204:207], v[172:175], v[28:31], v[204:207]
	v_mfma_f32_16x16x32_f16 v[236:239], v[132:135], v[28:31], v[236:239]
	s_waitcnt lgkmcnt(2)
	v_mfma_f32_16x16x32_f16 v[208:211], v[176:179], v[32:35], v[208:211]
	v_mfma_f32_16x16x32_f16 v[240:243], v[136:139], v[32:35], v[240:243]
	s_waitcnt lgkmcnt(1)
	v_mfma_f32_16x16x32_f16 v[212:215], v[180:183], v[36:39], v[212:215]
	v_mfma_f32_16x16x32_f16 v[244:247], v[140:143], v[36:39], v[244:247]
	s_waitcnt lgkmcnt(0)
	v_mfma_f32_16x16x32_f16 v[216:219], v[184:187], v[40:43], v[216:219]
	v_mfma_f32_16x16x32_f16 v[248:251], v[144:147], v[40:43], v[248:251]
	s_mov_b32 s40, 0x30000
	s_mov_b32 s41, 0x30400
	s_mov_b32 s42, 0x30800
	s_mov_b32 s43, 0x30c00
	s_mov_b32 s44, 0x31000
	buffer_load_dwordx4 v[148:151], v4, s[8:11], s40 offen
	buffer_load_dwordx4 v[152:155], v4, s[8:11], s41 offen
	buffer_load_dwordx4 v[156:159], v4, s[8:11], s42 offen
	buffer_load_dwordx4 v[160:163], v4, s[8:11], s43 offen
	buffer_load_dwordx4 v[164:167], v4, s[8:11], s44 offen
	s_mov_b32 s40, 0x31400
	s_mov_b32 s41, 0x31800
	s_mov_b32 s42, 0x31c00
	s_mov_b32 s43, 0x32000
	s_mov_b32 s44, 0x32400
	buffer_load_dwordx4 v[168:171], v4, s[8:11], s40 offen
	buffer_load_dwordx4 v[172:175], v4, s[8:11], s41 offen
	buffer_load_dwordx4 v[176:179], v4, s[8:11], s42 offen
	buffer_load_dwordx4 v[180:183], v4, s[8:11], s43 offen
	buffer_load_dwordx4 v[184:187], v4, s[8:11], s44 offen
	s_waitcnt vmcnt(34)
	v_cvt_pkrtz_f16_f32 v12, v44, v46
	v_cvt_pkrtz_f16_f32 v13, v48, v50
	v_cvt_pkrtz_f16_f32 v14, v52, v54
	v_cvt_pkrtz_f16_f32 v15, v56, v58
	v_cvt_pkrtz_f16_f32 v16, v45, v47
	v_cvt_pkrtz_f16_f32 v17, v49, v51
	v_cvt_pkrtz_f16_f32 v18, v53, v55
	v_cvt_pkrtz_f16_f32 v19, v57, v59
.Lpace_24:
	s_memrealtime s[54:55]
	s_waitcnt lgkmcnt(0)
	s_sub_u32 s54, s54, s52
	s_cmp_ge_u32 s54, 3520
	s_cbranch_scc1 .Lgo_24
	s_sleep 2
	s_branch .Lpace_24
.Lgo_24:
	s_mov_b32 s40, 0x1a470
	s_mov_b32 s41, 0x3c100
	s_mov_b32 s42, 0x5dd90
	s_mov_b32 s43, 0x7fa20
	s_mov_b32 s44, 0xa16b0
	s_mov_b32 s45, 0xc3340
	s_mov_b32 s46, 0xe4fd0
	s_mov_b32 s47, 0x106c60
	buffer_load_dwordx2 v[44:45], v3, s[4:7], s40 offen nt
	buffer_load_dwordx2 v[46:47], v3, s[4:7], s41 offen nt
	buffer_load_dwordx2 v[48:49], v3, s[4:7], s42 offen nt
	buffer_load_dwordx2 v[50:51], v3, s[4:7], s43 offen nt
	buffer_load_dwordx2 v[52:53], v3, s[4:7], s44 offen nt
	buffer_load_dwordx2 v[54:55], v3, s[4:7], s45 offen nt
	buffer_load_dwordx2 v[56:57], v3, s[4:7], s46 offen nt
	buffer_load_dwordx2 v[58:59], v3, s[4:7], s47 offen nt
	ds_write_b128 v5, v[12:15] offset:0
	ds_write_b128 v5, v[16:19] offset:2048
	s_waitcnt vmcnt(34)
	v_cvt_pkrtz_f16_f32 v12, v60, v62
	v_cvt_pkrtz_f16_f32 v13, v64, v66
	v_cvt_pkrtz_f16_f32 v14, v68, v70
	v_cvt_pkrtz_f16_f32 v15, v72, v74
	v_cvt_pkrtz_f16_f32 v16, v61, v63
	v_cvt_pkrtz_f16_f32 v17, v65, v67
	v_cvt_pkrtz_f16_f32 v18, v69, v71
	v_cvt_pkrtz_f16_f32 v19, v73, v75
.Lpace_25:
	s_memrealtime s[54:55]
	s_waitcnt lgkmcnt(0)
	s_sub_u32 s54, s54, s52
	s_cmp_ge_u32 s54, 3655
	s_cbranch_scc1 .Lgo_25
	s_sleep 2
	s_branch .Lpace_25
.Lgo_25:
	s_mov_b32 s40, 0x1288f0
	s_mov_b32 s41, 0x14a580
	s_mov_b32 s42, 0x16c210
	s_mov_b32 s43, 0x18dea0
	s_mov_b32 s44, 0x1afb30
	s_mov_b32 s45, 0x1d17c0
	s_mov_b32 s46, 0x1f3450
	s_mov_b32 s47, 0x2150e0
	buffer_load_dwordx2 v[60:61], v3, s[4:7], s40 offen nt
	buffer_load_dwordx2 v[62:63], v3, s[4:7], s41 offen nt
	buffer_load_dwordx2 v[64:65], v3, s[4:7], s42 offen nt
	buffer_load_dwordx2 v[66:67], v3, s[4:7], s43 offen nt
	buffer_load_dwordx2 v[68:69], v3, s[4:7], s44 offen nt
	buffer_load_dwordx2 v[70:71], v3, s[4:7], s45 offen nt
	buffer_load_dwordx2 v[72:73], v3, s[4:7], s46 offen nt
	buffer_load_dwordx2 v[74:75], v3, s[4:7], s47 offen nt
	ds_write_b128 v5, v[12:15] offset:256
	ds_write_b128 v5, v[16:19] offset:2304
	s_waitcnt vmcnt(34)
	v_cvt_pkrtz_f16_f32 v12, v76, v78
	v_cvt_pkrtz_f16_f32 v13, v80, v82
	v_cvt_pkrtz_f16_f32 v14, v84, v86
	v_cvt_pkrtz_f16_f32 v15, v88, v90
	v_cvt_pkrtz_f16_f32 v16, v77, v79
	v_cvt_pkrtz_f16_f32 v17, v81, v83
	v_cvt_pkrtz_f16_f32 v18, v85, v87
	v_cvt_pkrtz_f16_f32 v19, v89, v91
.Lpace_26:
	s_memrealtime s[54:55]
	s_waitcnt lgkmcnt(0)
	s_sub_u32 s54, s54, s52
	s_cmp_ge_u32 s54, 3790
	s_cbranch_scc1 .Lgo_26
	s_sleep 2
	s_branch .Lpace_26
.Lgo_26:
	s_mov_b32 s40, 0x236d70
	s_mov_b32 s41, 0x258a00
	s_mov_b32 s42, 0x27a690
	s_mov_b32 s43, 0x29c320
	s_mov_b32 s44, 0x2bdfb0
	s_mov_b32 s45, 0x2dfc40
	s_mov_b32 s46, 0x3018d0
	s_mov_b32 s47, 0x323560
	buffer_load_dwordx2 v[76:77], v3, s[4:7], s40 offen nt
	buffer_load_dwordx2 v[78:79], v3, s[4:7], s41 offen nt
	buffer_load_dwordx2 v[80:81], v3, s[4:7], s42 offen nt
	buffer_load_dwordx2 v[82:83], v3, s[4:7], s43 offen nt
	buffer_load_dwordx2 v[84:85], v3, s[4:7], s44 offen nt
	buffer_load_dwordx2 v[86:87], v3, s[4:7], s45 offen nt
	buffer_load_dwordx2 v[88:89], v3, s[4:7], s46 offen nt
	buffer_load_dwordx2 v[90:91], v3, s[4:7], s47 offen nt
	ds_write_b128 v5, v[12:15] offset:512
	ds_write_b128 v5, v[16:19] offset:2560
	s_waitcnt vmcnt(34)
	v_cvt_pkrtz_f16_f32 v12, v92, v94
	v_cvt_pkrtz_f16_f32 v13, v96, v98
	v_cvt_pkrtz_f16_f32 v14, v100, v102
	v_cvt_pkrtz_f16_f32 v15, v104, v106
	v_cvt_pkrtz_f16_f32 v16, v93, v95
	v_cvt_pkrtz_f16_f32 v17, v97, v99
	v_cvt_pkrtz_f16_f32 v18, v101, v103
	v_cvt_pkrtz_f16_f32 v19, v105, v107
.Lpace_27:
	s_memrealtime s[54:55]
	s_waitcnt lgkmcnt(0)
	s_sub_u32 s54, s54, s52
	s_cmp_ge_u32 s54, 3925
	s_cbranch_scc1 .Lgo_27
	s_sleep 2
	s_branch .Lpace_27
.Lgo_27:
	s_mov_b32 s40, 0x3451f0
	s_mov_b32 s41, 0x366e80
	s_mov_b32 s42, 0x388b10
	s_mov_b32 s43, 0x3aa7a0
	s_mov_b32 s44, 0x3cc430
	s_mov_b32 s45, 0x3ee0c0
	s_mov_b32 s46, 0x40fd50
	s_mov_b32 s47, 0x4319e0
	buffer_load_dwordx2 v[92:93], v3, s[4:7], s40 offen nt
	buffer_load_dwordx2 v[94:95], v3, s[4:7], s41 offen nt
	buffer_load_dwordx2 v[96:97], v3, s[4:7], s42 offen nt
	buffer_load_dwordx2 v[98:99], v3, s[4:7], s43 offen nt
	buffer_load_dwordx2 v[100:101], v3, s[4:7], s44 offen nt
	buffer_load_dwordx2 v[102:103], v3, s[4:7], s45 offen nt
	buffer_load_dwordx2 v[104:105], v3, s[4:7], s46 offen nt
	buffer_load_dwordx2 v[106:107], v3, s[4:7], s47 offen nt
	ds_write_b128 v5, v[12:15] offset:768
	ds_write_b128 v5, v[16:19] offset:2816
	s_waitcnt lgkmcnt(0)
	s_barrier
	ds_read_b128 v[12:15], v6 offset:0
	ds_read_b128 v[16:19], v6 offset:2048
	ds_read_b128 v[20:23], v7 offset:0
	ds_read_b128 v[24:27], v7 offset:2048
	ds_read_b128 v[28:31], v8 offset:0
	ds_read_b128 v[32:35], v8 offset:2048
	ds_read_b128 v[36:39], v9 offset:0
	ds_read_b128 v[40:43], v9 offset:2048
	s_waitcnt vmcnt(32)
	s_waitcnt lgkmcnt(7)
	v_mfma_f32_16x16x32_f16 v[188:191], v[108:111], v[12:15], v[188:191]
	v_mfma_f32_16x16x32_f16 v[220:223], v[148:151], v[12:15], v[220:223]
	s_waitcnt lgkmcnt(6)
	v_mfma_f32_16x16x32_f16 v[192:195], v[112:115], v[16:19], v[192:195]
	v_mfma_f32_16x16x32_f16 v[224:227], v[152:155], v[16:19], v[224:227]
	s_waitcnt lgkmcnt(5)
	v_mfma_f32_16x16x32_f16 v[196:199], v[116:119], v[20:23], v[196:199]
	v_mfma_f32_16x16x32_f16 v[228:231], v[156:159], v[20:23], v[228:231]
	s_waitcnt lgkmcnt(4)
	v_mfma_f32_16x16x32_f16 v[200:203], v[120:123], v[24:27], v[200:203]
	v_mfma_f32_16x16x32_f16 v[232:235], v[160:163], v[24:27], v[232:235]
	s_waitcnt lgkmcnt(3)
	v_mfma_f32_16x16x32_f16 v[204:207], v[124:127], v[28:31], v[204:207]
	v_mfma_f32_16x16x32_f16 v[236:239], v[164:167], v[28:31], v[236:239]
	s_waitcnt lgkmcnt(2)
	v_mfma_f32_16x16x32_f16 v[208:211], v[128:131], v[32:35], v[208:211]
	v_mfma_f32_16x16x32_f16 v[240:243], v[168:171], v[32:35], v[240:243]
	s_waitcnt lgkmcnt(1)
	v_mfma_f32_16x16x32_f16 v[212:215], v[132:135], v[36:39], v[212:215]
	v_mfma_f32_16x16x32_f16 v[244:247], v[172:175], v[36:39], v[244:247]
	s_waitcnt lgkmcnt(0)
	v_mfma_f32_16x16x32_f16 v[216:219], v[136:139], v[40:43], v[216:219]
	v_mfma_f32_16x16x32_f16 v[248:251], v[176:179], v[40:43], v[248:251]
	s_waitcnt vmcnt(24)
	v_cvt_pkrtz_f16_f32 v12, v44, v46
	v_cvt_pkrtz_f16_f32 v13, v48, v50
	v_cvt_pkrtz_f16_f32 v14, v52, v54
	v_cvt_pkrtz_f16_f32 v15, v56, v58
	v_cvt_pkrtz_f16_f32 v16, v45, v47
	v_cvt_pkrtz_f16_f32 v17, v49, v51
	v_cvt_pkrtz_f16_f32 v18, v53, v55
	v_cvt_pkrtz_f16_f32 v19, v57, v59
.Lpace_28:
	s_memrealtime s[54:55]
	s_waitcnt lgkmcnt(0)
	s_sub_u32 s54, s54, s52
	s_cmp_ge_u32 s54, 4060
	s_cbranch_scc1 .Lgo_28
	s_sleep 2
	s_branch .Lpace_28
.Lgo_28:
	s_mov_b32 s40, 0x1e080
	s_mov_b32 s41, 0x3fd10
	s_mov_b32 s42, 0x619a0
	s_mov_b32 s43, 0x83630
	s_mov_b32 s44, 0xa52c0
	s_mov_b32 s45, 0xc6f50
	s_mov_b32 s46, 0xe8be0
	s_mov_b32 s47, 0x10a870
	buffer_load_dwordx2 v[44:45], v3, s[4:7], s40 offen nt
	buffer_load_dwordx2 v[46:47], v3, s[4:7], s41 offen nt
	buffer_load_dwordx2 v[48:49], v3, s[4:7], s42 offen nt
	buffer_load_dwordx2 v[50:51], v3, s[4:7], s43 offen nt
	buffer_load_dwordx2 v[52:53], v3, s[4:7], s44 offen nt
	buffer_load_dwordx2 v[54:55], v3, s[4:7], s45 offen nt
	buffer_load_dwordx2 v[56:57], v3, s[4:7], s46 offen nt
	buffer_load_dwordx2 v[58:59], v3, s[4:7], s47 offen nt
	ds_write_b128 v5, v[12:15] offset:1024
	ds_write_b128 v5, v[16:19] offset:3072
	s_waitcnt vmcnt(24)
	v_cvt_pkrtz_f16_f32 v12, v60, v62
	v_cvt_pkrtz_f16_f32 v13, v64, v66
	v_cvt_pkrtz_f16_f32 v14, v68, v70
	v_cvt_pkrtz_f16_f32 v15, v72, v74
	v_cvt_pkrtz_f16_f32 v16, v61, v63
	v_cvt_pkrtz_f16_f32 v17, v65, v67
	v_cvt_pkrtz_f16_f32 v18, v69, v71
	v_cvt_pkrtz_f16_f32 v19, v73, v75
.Lpace_29:
	s_memrealtime s[54:55]
	s_waitcnt lgkmcnt(0)
	s_sub_u32 s54, s54, s52
	s_cmp_ge_u32 s54, 4195
	s_cbranch_scc1 .Lgo_29
	s_sleep 2
	s_branch .Lpace_29
.Lgo_29:
	s_mov_b32 s40, 0x12c500
	s_mov_b32 s41, 0x14e190
	s_mov_b32 s42, 0x16fe20
	s_mov_b32 s43, 0x191ab0
	s_mov_b32 s44, 0x1b3740
	s_mov_b32 s45, 0x1d53d0
	s_mov_b32 s46, 0x1f7060
	s_mov_b32 s47, 0x218cf0
	buffer_load_dwordx2 v[60:61], v3, s[4:7], s40 offen nt
	buffer_load_dwordx2 v[62:63], v3, s[4:7], s41 offen nt
	buffer_load_dwordx2 v[64:65], v3, s[4:7], s42 offen nt
	buffer_load_dwordx2 v[66:67], v3, s[4:7], s43 offen nt
	buffer_load_dwordx2 v[68:69], v3, s[4:7], s44 offen nt
	buffer_load_dwordx2 v[70:71], v3, s[4:7], s45 offen nt
	buffer_load_dwordx2 v[72:73], v3, s[4:7], s46 offen nt
	buffer_load_dwordx2 v[74:75], v3, s[4:7], s47 offen nt
	ds_write_b128 v5, v[12:15] offset:1280
	ds_write_b128 v5, v[16:19] offset:3328
	s_waitcnt vmcnt(24)
	v_cvt_pkrtz_f16_f32 v12, v76, v78
	v_cvt_pkrtz_f16_f32 v13, v80, v82
	v_cvt_pkrtz_f16_f32 v14, v84, v86
	v_cvt_pkrtz_f16_f32 v15, v88, v90
	v_cvt_pkrtz_f16_f32 v16, v77, v79
	v_cvt_pkrtz_f16_f32 v17, v81, v83
	v_cvt_pkrtz_f16_f32 v18, v85, v87
	v_cvt_pkrtz_f16_f32 v19, v89, v91
.Lpace_30:
	s_memrealtime s[54:55]
	s_waitcnt lgkmcnt(0)
	s_sub_u32 s54, s54, s52
	s_cmp_ge_u32 s54, 4330
	s_cbranch_scc1 .Lgo_30
	s_sleep 2
	s_branch .Lpace_30
.Lgo_30:
	s_mov_b32 s40, 0x23a980
	s_mov_b32 s41, 0x25c610
	s_mov_b32 s42, 0x27e2a0
	s_mov_b32 s43, 0x29ff30
	s_mov_b32 s44, 0x2c1bc0
	s_mov_b32 s45, 0x2e3850
	s_mov_b32 s46, 0x3054e0
	s_mov_b32 s47, 0x327170
	buffer_load_dwordx2 v[76:77], v3, s[4:7], s40 offen nt
	buffer_load_dwordx2 v[78:79], v3, s[4:7], s41 offen nt
	buffer_load_dwordx2 v[80:81], v3, s[4:7], s42 offen nt
	buffer_load_dwordx2 v[82:83], v3, s[4:7], s43 offen nt
	buffer_load_dwordx2 v[84:85], v3, s[4:7], s44 offen nt
	buffer_load_dwordx2 v[86:87], v3, s[4:7], s45 offen nt
	buffer_load_dwordx2 v[88:89], v3, s[4:7], s46 offen nt
	buffer_load_dwordx2 v[90:91], v3, s[4:7], s47 offen nt
	ds_write_b128 v5, v[12:15] offset:1536
	ds_write_b128 v5, v[16:19] offset:3584
	s_waitcnt vmcnt(24)
	v_cvt_pkrtz_f16_f32 v12, v92, v94
	v_cvt_pkrtz_f16_f32 v13, v96, v98
	v_cvt_pkrtz_f16_f32 v14, v100, v102
	v_cvt_pkrtz_f16_f32 v15, v104, v106
	v_cvt_pkrtz_f16_f32 v16, v93, v95
	v_cvt_pkrtz_f16_f32 v17, v97, v99
	v_cvt_pkrtz_f16_f32 v18, v101, v103
	v_cvt_pkrtz_f16_f32 v19, v105, v107
.Lpace_31:
	s_memrealtime s[54:55]
	s_waitcnt lgkmcnt(0)
	s_sub_u32 s54, s54, s52
	s_cmp_ge_u32 s54, 4465
	s_cbranch_scc1 .Lgo_31
	s_sleep 2
	s_branch .Lpace_31
.Lgo_31:
	s_mov_b32 s40, 0x348e00
	s_mov_b32 s41, 0x36aa90
	s_mov_b32 s42, 0x38c720
	s_mov_b32 s43, 0x3ae3b0
	s_mov_b32 s44, 0x3d0040
	s_mov_b32 s45, 0x3f1cd0
	s_mov_b32 s46, 0x413960
	s_mov_b32 s47, 0x4355f0
	buffer_load_dwordx2 v[92:93], v3, s[4:7], s40 offen nt
	buffer_load_dwordx2 v[94:95], v3, s[4:7], s41 offen nt
	buffer_load_dwordx2 v[96:97], v3, s[4:7], s42 offen nt
	buffer_load_dwordx2 v[98:99], v3, s[4:7], s43 offen nt
	buffer_load_dwordx2 v[100:101], v3, s[4:7], s44 offen nt
	buffer_load_dwordx2 v[102:103], v3, s[4:7], s45 offen nt
	buffer_load_dwordx2 v[104:105], v3, s[4:7], s46 offen nt
	buffer_load_dwordx2 v[106:107], v3, s[4:7], s47 offen nt
	ds_write_b128 v5, v[12:15] offset:1792
	ds_write_b128 v5, v[16:19] offset:3840
	s_waitcnt lgkmcnt(0)
	s_barrier
	ds_read_b128 v[12:15], v6 offset:1024
	ds_read_b128 v[16:19], v6 offset:3072
	ds_read_b128 v[20:23], v7 offset:1024
	ds_read_b128 v[24:27], v7 offset:3072
	ds_read_b128 v[28:31], v8 offset:1024
	ds_read_b128 v[32:35], v8 offset:3072
	ds_read_b128 v[36:39], v9 offset:1024
	ds_read_b128 v[40:43], v9 offset:3072
	s_waitcnt lgkmcnt(7)
	v_mfma_f32_16x16x32_f16 v[188:191], v[112:115], v[12:15], v[188:191]
	v_mfma_f32_16x16x32_f16 v[220:223], v[152:155], v[12:15], v[220:223]
	s_waitcnt lgkmcnt(6)
	v_mfma_f32_16x16x32_f16 v[192:195], v[116:119], v[16:19], v[192:195]
	v_mfma_f32_16x16x32_f16 v[224:227], v[156:159], v[16:19], v[224:227]
	s_waitcnt lgkmcnt(5)
	v_mfma_f32_16x16x32_f16 v[196:199], v[120:123], v[20:23], v[196:199]
	v_mfma_f32_16x16x32_f16 v[228:231], v[160:163], v[20:23], v[228:231]
	s_waitcnt lgkmcnt(4)
	v_mfma_f32_16x16x32_f16 v[200:203], v[124:127], v[24:27], v[200:203]
	v_mfma_f32_16x16x32_f16 v[232:235], v[164:167], v[24:27], v[232:235]
	s_waitcnt lgkmcnt(3)
	v_mfma_f32_16x16x32_f16 v[204:207], v[128:131], v[28:31], v[204:207]
	v_mfma_f32_16x16x32_f16 v[236:239], v[168:171], v[28:31], v[236:239]
	s_waitcnt lgkmcnt(2)
	v_mfma_f32_16x16x32_f16 v[208:211], v[132:135], v[32:35], v[208:211]
	v_mfma_f32_16x16x32_f16 v[240:243], v[172:175], v[32:35], v[240:243]
	s_waitcnt lgkmcnt(1)
	v_mfma_f32_16x16x32_f16 v[212:215], v[136:139], v[36:39], v[212:215]
	v_mfma_f32_16x16x32_f16 v[244:247], v[176:179], v[36:39], v[244:247]
	s_waitcnt lgkmcnt(0)
	v_mfma_f32_16x16x32_f16 v[216:219], v[140:143], v[40:43], v[216:219]
	v_mfma_f32_16x16x32_f16 v[248:251], v[180:183], v[40:43], v[248:251]
	s_waitcnt vmcnt(24)
	v_cvt_pkrtz_f16_f32 v12, v44, v46
	v_cvt_pkrtz_f16_f32 v13, v48, v50
	v_cvt_pkrtz_f16_f32 v14, v52, v54
	v_cvt_pkrtz_f16_f32 v15, v56, v58
	v_cvt_pkrtz_f16_f32 v16, v45, v47
	v_cvt_pkrtz_f16_f32 v17, v49, v51
	v_cvt_pkrtz_f16_f32 v18, v53, v55
	v_cvt_pkrtz_f16_f32 v19, v57, v59
	ds_write_b128 v5, v[12:15] offset:0
	ds_write_b128 v5, v[16:19] offset:2048
	s_waitcnt vmcnt(16)
	v_cvt_pkrtz_f16_f32 v12, v60, v62
	v_cvt_pkrtz_f16_f32 v13, v64, v66
	v_cvt_pkrtz_f16_f32 v14, v68, v70
	v_cvt_pkrtz_f16_f32 v15, v72, v74
	v_cvt_pkrtz_f16_f32 v16, v61, v63
	v_cvt_pkrtz_f16_f32 v17, v65, v67
	v_cvt_pkrtz_f16_f32 v18, v69, v71
	v_cvt_pkrtz_f16_f32 v19, v73, v75
	ds_write_b128 v5, v[12:15] offset:256
	ds_write_b128 v5, v[16:19] offset:2304
	s_waitcnt vmcnt(8)
	v_cvt_pkrtz_f16_f32 v12, v76, v78
	v_cvt_pkrtz_f16_f32 v13, v80, v82
	v_cvt_pkrtz_f16_f32 v14, v84, v86
	v_cvt_pkrtz_f16_f32 v15, v88, v90
	v_cvt_pkrtz_f16_f32 v16, v77, v79
	v_cvt_pkrtz_f16_f32 v17, v81, v83
	v_cvt_pkrtz_f16_f32 v18, v85, v87
	v_cvt_pkrtz_f16_f32 v19, v89, v91
	ds_write_b128 v5, v[12:15] offset:512
	ds_write_b128 v5, v[16:19] offset:2560
	s_waitcnt vmcnt(0)
	v_cvt_pkrtz_f16_f32 v12, v92, v94
	v_cvt_pkrtz_f16_f32 v13, v96, v98
	v_cvt_pkrtz_f16_f32 v14, v100, v102
	v_cvt_pkrtz_f16_f32 v15, v104, v106
	v_cvt_pkrtz_f16_f32 v16, v93, v95
	v_cvt_pkrtz_f16_f32 v17, v97, v99
	v_cvt_pkrtz_f16_f32 v18, v101, v103
	v_cvt_pkrtz_f16_f32 v19, v105, v107
	ds_write_b128 v5, v[12:15] offset:768
	ds_write_b128 v5, v[16:19] offset:2816
	s_waitcnt lgkmcnt(0)
	s_barrier
	ds_read_b128 v[12:15], v6 offset:0
	ds_read_b128 v[16:19], v6 offset:2048
	ds_read_b128 v[20:23], v7 offset:0
	ds_read_b128 v[24:27], v7 offset:2048
	ds_read_b128 v[28:31], v8 offset:0
	ds_read_b128 v[32:35], v8 offset:2048
	ds_read_b128 v[36:39], v9 offset:0
	ds_read_b128 v[40:43], v9 offset:2048
	s_waitcnt lgkmcnt(7)
	v_mfma_f32_16x16x32_f16 v[188:191], v[116:119], v[12:15], v[188:191]
	v_mfma_f32_16x16x32_f16 v[220:223], v[156:159], v[12:15], v[220:223]
	s_waitcnt lgkmcnt(6)
	v_mfma_f32_16x16x32_f16 v[192:195], v[120:123], v[16:19], v[192:195]
	v_mfma_f32_16x16x32_f16 v[224:227], v[160:163], v[16:19], v[224:227]
	s_waitcnt lgkmcnt(5)
	v_mfma_f32_16x16x32_f16 v[196:199], v[124:127], v[20:23], v[196:199]
	v_mfma_f32_16x16x32_f16 v[228:231], v[164:167], v[20:23], v[228:231]
	s_waitcnt lgkmcnt(4)
	v_mfma_f32_16x16x32_f16 v[200:203], v[128:131], v[24:27], v[200:203]
	v_mfma_f32_16x16x32_f16 v[232:235], v[168:171], v[24:27], v[232:235]
	s_waitcnt lgkmcnt(3)
	v_mfma_f32_16x16x32_f16 v[204:207], v[132:135], v[28:31], v[204:207]
	v_mfma_f32_16x16x32_f16 v[236:239], v[172:175], v[28:31], v[236:239]
	s_waitcnt lgkmcnt(2)
	v_mfma_f32_16x16x32_f16 v[208:211], v[136:139], v[32:35], v[208:211]
	v_mfma_f32_16x16x32_f16 v[240:243], v[176:179], v[32:35], v[240:243]
	s_waitcnt lgkmcnt(1)
	v_mfma_f32_16x16x32_f16 v[212:215], v[140:143], v[36:39], v[212:215]
	v_mfma_f32_16x16x32_f16 v[244:247], v[180:183], v[36:39], v[244:247]
	s_waitcnt lgkmcnt(0)
	v_mfma_f32_16x16x32_f16 v[216:219], v[144:147], v[40:43], v[216:219]
	v_mfma_f32_16x16x32_f16 v[248:251], v[184:187], v[40:43], v[248:251]
	s_nop 7
	s_nop 3
	v_and_b32_e32 v10, 1, v0
	v_cmp_eq_u32_e32 vcc, 1, v10
	s_nop 1
	v_cndmask_b32_e32 v188, v188, v220, vcc
	v_cndmask_b32_e32 v189, v189, v221, vcc
	v_cndmask_b32_e32 v190, v190, v222, vcc
	v_cndmask_b32_e32 v191, v191, v223, vcc
	v_cndmask_b32_e32 v192, v192, v224, vcc
	v_cndmask_b32_e32 v193, v193, v225, vcc
	v_cndmask_b32_e32 v194, v194, v226, vcc
	v_cndmask_b32_e32 v195, v195, v227, vcc
	v_cndmask_b32_e32 v196, v196, v228, vcc
	v_cndmask_b32_e32 v197, v197, v229, vcc
	v_cndmask_b32_e32 v198, v198, v230, vcc
	v_cndmask_b32_e32 v199, v199, v231, vcc
	v_cndmask_b32_e32 v200, v200, v232, vcc
	v_cndmask_b32_e32 v201, v201, v233, vcc
	v_cndmask_b32_e32 v202, v202, v234, vcc
	v_cndmask_b32_e32 v203, v203, v235, vcc
	v_cndmask_b32_e32 v204, v204, v236, vcc
	v_cndmask_b32_e32 v205, v205, v237, vcc
	v_cndmask_b32_e32 v206, v206, v238, vcc
	v_cndmask_b32_e32 v207, v207, v239, vcc
	v_cndmask_b32_e32 v208, v208, v240, vcc
	v_cndmask_b32_e32 v209, v209, v241, vcc
	v_cndmask_b32_e32 v210, v210, v242, vcc
	v_cndmask_b32_e32 v211, v211, v243, vcc
	v_cndmask_b32_e32 v212, v212, v244, vcc
	v_cndmask_b32_e32 v213, v213, v245, vcc
	v_cndmask_b32_e32 v214, v214, v246, vcc
	v_cndmask_b32_e32 v215, v215, v247, vcc
	v_cndmask_b32_e32 v216, v216, v248, vcc
	v_cndmask_b32_e32 v217, v217, v249, vcc
	v_cndmask_b32_e32 v218, v218, v250, vcc
	v_cndmask_b32_e32 v219, v219, v251, vcc
	s_barrier
	v_lshrrev_b32_e32 v10, 4, v2
	v_lshlrev_b32_e32 v10, 6, v10
	v_and_b32_e32 v12, 15, v2
	v_add_u32_e32 v10, v10, v12
	v_mul_u32_u24_e32 v10, 0x108, v10
	v_lshl_add_u32 v10, v1, 5, v10
	ds_write_b32 v10, v188 offset:0
	ds_write_b32 v10, v189 offset:4224
	ds_write_b32 v10, v190 offset:8448
	ds_write_b32 v10, v191 offset:12672
	ds_write_b32 v10, v192 offset:4
	ds_write_b32 v10, v193 offset:4228
	ds_write_b32 v10, v194 offset:8452
	ds_write_b32 v10, v195 offset:12676
	s_waitcnt lgkmcnt(4)
	ds_write_b32 v10, v196 offset:8
	ds_write_b32 v10, v197 offset:4232
	ds_write_b32 v10, v198 offset:8456
	ds_write_b32 v10, v199 offset:12680
	ds_write_b32 v10, v200 offset:12
	ds_write_b32 v10, v201 offset:4236
	ds_write_b32 v10, v202 offset:8460
	ds_write_b32 v10, v203 offset:12684
	s_waitcnt lgkmcnt(4)
	ds_write_b32 v10, v204 offset:16
	ds_write_b32 v10, v205 offset:4240
	ds_write_b32 v10, v206 offset:8464
	ds_write_b32 v10, v207 offset:12688
	ds_write_b32 v10, v208 offset:20
	ds_write_b32 v10, v209 offset:4244
	ds_write_b32 v10, v210 offset:8468
	ds_write_b32 v10, v211 offset:12692
	s_waitcnt lgkmcnt(4)
	ds_write_b32 v10, v212 offset:24
	ds_write_b32 v10, v213 offset:4248
	ds_write_b32 v10, v214 offset:8472
	ds_write_b32 v10, v215 offset:12696
	ds_write_b32 v10, v216 offset:28
	ds_write_b32 v10, v217 offset:4252
	ds_write_b32 v10, v218 offset:8476
	ds_write_b32 v10, v219 offset:12700
	s_waitcnt lgkmcnt(0)
	s_barrier
	v_lshrrev_b32_e32 v12, 5, v0
	v_mul_u32_u24_e32 v12, 0x108, v12
	v_and_b32_e32 v13, 31, v0
	v_lshl_add_u32 v12, v13, 3, v12
	ds_read_b64 v[44:45], v12 offset:0
	ds_read_b64 v[46:47], v12 offset:4224
	ds_read_b64 v[48:49], v12 offset:8448
	ds_read_b64 v[50:51], v12 offset:12672
	ds_read_b64 v[52:53], v12 offset:16896
	ds_read_b64 v[54:55], v12 offset:21120
	ds_read_b64 v[56:57], v12 offset:25344
	ds_read_b64 v[58:59], v12 offset:29568
	s_waitcnt lgkmcnt(7)
	v_add_f32_e32 v44, v252, v44
	v_add_f32_e32 v45, v253, v45
	s_mov_b32 s40, 0x0
	buffer_store_dwordx2 v[44:45], v11, s[32:35], s40 offen nt
	s_waitcnt lgkmcnt(6)
	v_add_f32_e32 v46, v252, v46
	v_add_f32_e32 v47, v253, v47
	s_mov_b32 s41, 0xf0400
	buffer_store_dwordx2 v[46:47], v11, s[32:35], s41 offen nt
	s_waitcnt lgkmcnt(5)
	v_add_f32_e32 v48, v252, v48
	v_add_f32_e32 v49, v253, v49
	s_mov_b32 s42, 0x1e0800
	buffer_store_dwordx2 v[48:49], v11, s[32:35], s42 offen nt
	s_waitcnt lgkmcnt(4)
	v_add_f32_e32 v50, v252, v50
	v_add_f32_e32 v51, v253, v51
	s_mov_b32 s43, 0x2d0c00
	buffer_store_dwordx2 v[50:51], v11, s[32:35], s43 offen nt
	s_waitcnt lgkmcnt(3)
	v_add_f32_e32 v52, v252, v52
	v_add_f32_e32 v53, v253, v53
	s_mov_b32 s44, 0x3c1000
	buffer_store_dwordx2 v[52:53], v11, s[32:35], s44 offen nt
	s_waitcnt lgkmcnt(2)
	v_add_f32_e32 v54, v252, v54
	v_add_f32_e32 v55, v253, v55
	s_mov_b32 s45, 0x4b1400
	buffer_store_dwordx2 v[54:55], v11, s[32:35], s45 offen nt
	s_waitcnt lgkmcnt(1)
	v_add_f32_e32 v56, v252, v56
	v_add_f32_e32 v57, v253, v57
	s_mov_b32 s46, 0x5a1800
	buffer_store_dwordx2 v[56:57], v11, s[32:35], s46 offen nt
	s_waitcnt lgkmcnt(0)
	v_add_f32_e32 v58, v252, v58
	v_add_f32_e32 v59, v253, v59
	s_mov_b32 s47, 0x691c00
	buffer_store_dwordx2 v[58:59], v11, s[32:35], s47 offen nt
	ds_read_b64 v[60:61], v12 offset:33792
	ds_read_b64 v[62:63], v12 offset:38016
	ds_read_b64 v[64:65], v12 offset:42240
	ds_read_b64 v[66:67], v12 offset:46464
	ds_read_b64 v[68:69], v12 offset:50688
	ds_read_b64 v[70:71], v12 offset:54912
	ds_read_b64 v[72:73], v12 offset:59136
	ds_read_b64 v[74:75], v12 offset:63360
	s_waitcnt lgkmcnt(7)
	v_add_f32_e32 v60, v252, v60
	v_add_f32_e32 v61, v253, v61
	s_mov_b32 s40, 0x782000
	buffer_store_dwordx2 v[60:61], v11, s[32:35], s40 offen nt
	s_waitcnt lgkmcnt(6)
	v_add_f32_e32 v62, v252, v62
	v_add_f32_e32 v63, v253, v63
	s_mov_b32 s41, 0x872400
	buffer_store_dwordx2 v[62:63], v11, s[32:35], s41 offen nt
	s_waitcnt lgkmcnt(5)
	v_add_f32_e32 v64, v252, v64
	v_add_f32_e32 v65, v253, v65
	s_mov_b32 s42, 0x962800
	buffer_store_dwordx2 v[64:65], v11, s[32:35], s42 offen nt
	s_waitcnt lgkmcnt(4)
	v_add_f32_e32 v66, v252, v66
	v_add_f32_e32 v67, v253, v67
	s_mov_b32 s43, 0xa52c00
	buffer_store_dwordx2 v[66:67], v11, s[32:35], s43 offen nt
	s_waitcnt lgkmcnt(3)
	v_add_f32_e32 v68, v252, v68
	v_add_f32_e32 v69, v253, v69
	s_mov_b32 s44, 0xb43000
	buffer_store_dwordx2 v[68:69], v11, s[32:35], s44 offen nt
	s_waitcnt lgkmcnt(2)
	v_add_f32_e32 v70, v252, v70
	v_add_f32_e32 v71, v253, v71
	s_mov_b32 s45, 0xc33400
	buffer_store_dwordx2 v[70:71], v11, s[32:35], s45 offen nt
	s_waitcnt lgkmcnt(1)
	v_add_f32_e32 v72, v252, v72
	v_add_f32_e32 v73, v253, v73
	s_mov_b32 s46, 0xd23800
	buffer_store_dwordx2 v[72:73], v11, s[32:35], s46 offen nt
	s_waitcnt lgkmcnt(0)
	v_add_f32_e32 v74, v252, v74
	v_add_f32_e32 v75, v253, v75
	s_mov_b32 s47, 0xe13c00
	buffer_store_dwordx2 v[74:75], v11, s[32:35], s47 offen nt
	s_endpgm
